# speedup vs baseline: 1.0404x; 1.0404x over previous
.LBB3_32:
	s_or_b64 exec, exec, s[8:9]
	v_bfe_u32 v158, v0, 6, 1
	v_lshrrev_b32_e32 v5, 1, v0
	v_and_b32_e32 v8, 31, v0
	v_lshlrev_b32_e32 v157, 6, v158
	v_and_b32_e32 v5, 0xc0, v5
	v_or_b32_e32 v9, v157, v8
	v_lshrrev_b32_e32 v7, 5, v0
	v_bfe_u32 v150, v0, 5, 1
	v_or_b32_e32 v149, v5, v8
	v_bfe_u32 v10, v0, 2, 2
	v_lshlrev_b32_e32 v9, 2, v9
	v_add_u32_e32 v14, 1, v8
	v_add_u32_e32 v8, 2, v8
	v_bitop3_b32 v7, v7, v10, 1 bitop3:0x6c
	v_bitop3_b32 v12, v150, v10, 2 bitop3:0x36
	v_or_b32_e32 v15, v14, v5
	v_or_b32_e32 v16, v8, v5
	v_or_b32_e32 v5, 0x400, v9
	v_or_b32_e32 v151, 2, v150
	v_or_b32_e32 v17, v5, v7
	v_or_b32_e32 v18, v5, v12
	v_or_b32_e32 v5, 0x480, v9
	v_bitop3_b32 v11, v9, v150, v10 bitop3:0xf6
	v_bitop3_b32 v13, v9, v151, v10 bitop3:0xf6
	v_or_b32_e32 v9, v5, v7
	v_or_b32_e32 v12, v5, v12
	v_lshlrev_b32_e32 v5, 2, v149
	v_bitop3_b32 v184, v150, v5, v10 bitop3:0xde
	v_bitop3_b32 v183, v151, v5, v10 bitop3:0xde
	v_mov_b32_e32 v10, 0x1f700
	v_mov_b32_e32 v5, 0x13700
	v_lshl_add_u32 v182, v3, 4, v10
	v_mov_b32_e32 v3, 0
	v_lshl_add_u32 v165, v11, 4, v5
	v_lshl_add_u32 v166, v13, 4, v5
	v_cmp_lt_i32_e64 s[6:7], -1, v2
	v_lshl_add_u64 v[136:137], v[2:3], 2, s[24:25]
	v_bfe_u32 v2, v14, 2, 2
	v_lshlrev_b32_e32 v5, 2, v15
	v_bitop3_b32 v180, v2, v5, v150 bitop3:0xde
	v_bitop3_b32 v179, v2, v5, v151 bitop3:0xde
	v_bfe_u32 v2, v8, 2, 2
	v_lshlrev_b32_e32 v5, 2, v16
	v_bitop3_b32 v178, v2, v5, v150 bitop3:0xde
	v_bitop3_b32 v177, v2, v5, v151 bitop3:0xde
	v_add_u32_e32 v2, 0xb6, v149
	v_bfe_u32 v5, v2, 2, 2
	v_lshlrev_b32_e32 v2, 2, v2
	v_bitop3_b32 v176, v5, v2, v150 bitop3:0xde
	v_bitop3_b32 v175, v5, v2, v151 bitop3:0xde
	v_add_u32_e32 v2, 0xb6, v15
	v_bfe_u32 v5, v2, 2, 2
	v_lshlrev_b32_e32 v2, 2, v2
	v_bitop3_b32 v174, v5, v2, v150 bitop3:0xde
	v_bitop3_b32 v173, v5, v2, v151 bitop3:0xde
	v_add_u32_e32 v2, 0xb6, v16
	v_bfe_u32 v5, v2, 2, 2
	v_lshlrev_b32_e32 v2, 2, v2
	v_bitop3_b32 v172, v5, v2, v150 bitop3:0xde
	v_bitop3_b32 v171, v5, v2, v151 bitop3:0xde
	v_add_u32_e32 v2, 0x16c, v149
	v_bfe_u32 v5, v2, 2, 2
	v_lshlrev_b32_e32 v2, 2, v2
	v_mov_b32_e32 v7, v3
	v_bitop3_b32 v170, v5, v2, v150 bitop3:0xde
	v_bitop3_b32 v169, v5, v2, v151 bitop3:0xde
	v_add_u32_e32 v2, 0x16c, v15
	v_cmp_lt_i32_e64 s[8:9], -1, v6
	v_lshl_add_u64 v[138:139], v[6:7], 2, s[24:25]
	v_bfe_u32 v6, v2, 2, 2
	v_lshlrev_b32_e32 v2, 2, v2
	s_waitcnt lgkmcnt(0)
	v_bitop3_b32 v168, v6, v2, v150 bitop3:0xde
	v_bitop3_b32 v167, v6, v2, v151 bitop3:0xde
	v_add_u32_e32 v2, 0x16c, v16
	s_add_u32 s12, s12, s27
	v_mov_b32_e32 v5, v3
	v_bfe_u32 v6, v2, 2, 2
	v_lshlrev_b32_e32 v2, 2, v2
	s_addc_u32 s13, s13, s26
	v_add_u32_e32 v181, 0x13700, v142
	v_lshrrev_b32_e32 v148, 2, v0
	v_bitop3_b32 v164, v6, v2, v150 bitop3:0xde
	v_bitop3_b32 v163, v6, v2, v151 bitop3:0xde
	v_lshl_add_u32 v161, v17, 4, v10
	v_lshl_add_u32 v162, v18, 4, v10
	v_lshl_add_u32 v159, v9, 4, v10
	v_lshl_add_u32 v160, v12, 4, v10
	v_lshl_add_u64 v[140:141], v[4:5], 2, s[12:13]
	v_mov_b32_e32 v135, v3
	v_mov_b32_e32 v133, v3
	v_mov_b32_e32 v131, v3
	s_mov_b32 s31, 0
	s_mov_b64 s[40:41], s[12:13]
	s_mov_b64 s[12:13], 0
	s_mov_b32 s30, 0x38800000
	s_mov_b64 s[16:17], 0xc000
	s_mov_b64 s[18:19], 0x12000
	s_mov_b64 s[24:25], 0x18000
	s_xor_b64 s[10:11], s[10:11], -1
	v_mov_b32_e32 v2, v3
	v_mov_b32_e32 v4, v3
	v_mov_b32_e32 v6, v3
	v_mov_b32_e32 v8, v3
	v_mov_b32_e32 v9, v3
	v_mov_b32_e32 v10, v3
	v_mov_b32_e32 v11, v3
	v_mov_b32_e32 v12, v3
	v_mov_b32_e32 v13, v3
	v_mov_b32_e32 v14, v3
	v_mov_b32_e32 v15, v3
	v_mov_b32_e32 v16, v3
	v_mov_b32_e32 v17, v3
	v_mov_b32_e32 v34, v3
	v_mov_b32_e32 v35, v3
	v_mov_b32_e32 v36, v3
	v_mov_b32_e32 v37, v3
	v_mov_b32_e32 v38, v3
	v_mov_b32_e32 v39, v3
	v_mov_b32_e32 v40, v3
	v_mov_b32_e32 v41, v3
	v_mov_b32_e32 v42, v3
	v_mov_b32_e32 v43, v3
	v_mov_b32_e32 v44, v3
	v_mov_b32_e32 v45, v3
	v_mov_b32_e32 v46, v3
	v_mov_b32_e32 v47, v3
	v_mov_b32_e32 v48, v3
	v_mov_b32_e32 v49, v3
	v_mov_b32_e32 v66, v3
	v_mov_b32_e32 v67, v3
	v_mov_b32_e32 v68, v3
	v_mov_b32_e32 v69, v3
	v_mov_b32_e32 v70, v3
	v_mov_b32_e32 v71, v3
	v_mov_b32_e32 v72, v3
	v_mov_b32_e32 v73, v3
	v_mov_b32_e32 v74, v3
	v_mov_b32_e32 v75, v3
	v_mov_b32_e32 v76, v3
	v_mov_b32_e32 v77, v3
	v_mov_b32_e32 v78, v3
	v_mov_b32_e32 v79, v3
	v_mov_b32_e32 v80, v3
	v_mov_b32_e32 v81, v3
	v_mov_b32_e32 v98, v3
	v_mov_b32_e32 v99, v3
	v_mov_b32_e32 v100, v3
	v_mov_b32_e32 v101, v3
	v_mov_b32_e32 v102, v3
	v_mov_b32_e32 v103, v3
	v_mov_b32_e32 v104, v3
	v_mov_b32_e32 v105, v3
	v_mov_b32_e32 v106, v3
	v_mov_b32_e32 v107, v3
	v_mov_b32_e32 v108, v3
	v_mov_b32_e32 v109, v3
	v_mov_b32_e32 v110, v3
	v_mov_b32_e32 v111, v3
	v_mov_b32_e32 v112, v3
	v_mov_b32_e32 v113, v3
	v_mov_b32_e32 v18, v3
	v_mov_b32_e32 v19, v3
	v_mov_b32_e32 v20, v3
	v_mov_b32_e32 v21, v3
	v_mov_b32_e32 v22, v3
	v_mov_b32_e32 v23, v3
	v_mov_b32_e32 v24, v3
	v_mov_b32_e32 v25, v3
	v_mov_b32_e32 v26, v3
	v_mov_b32_e32 v27, v3
	v_mov_b32_e32 v28, v3
	v_mov_b32_e32 v29, v3
	v_mov_b32_e32 v30, v3
	v_mov_b32_e32 v31, v3
	v_mov_b32_e32 v32, v3
	v_mov_b32_e32 v33, v3
	v_mov_b32_e32 v50, v3
	v_mov_b32_e32 v51, v3
	v_mov_b32_e32 v52, v3
	v_mov_b32_e32 v53, v3
	v_mov_b32_e32 v54, v3
	v_mov_b32_e32 v55, v3
	v_mov_b32_e32 v56, v3
	v_mov_b32_e32 v57, v3
	v_mov_b32_e32 v58, v3
	v_mov_b32_e32 v59, v3
	v_mov_b32_e32 v60, v3
	v_mov_b32_e32 v61, v3
	v_mov_b32_e32 v62, v3
	v_mov_b32_e32 v63, v3
	v_mov_b32_e32 v64, v3
	v_mov_b32_e32 v65, v3
	v_mov_b32_e32 v82, v3
	v_mov_b32_e32 v83, v3
	v_mov_b32_e32 v84, v3
	v_mov_b32_e32 v85, v3
	v_mov_b32_e32 v86, v3
	v_mov_b32_e32 v87, v3
	v_mov_b32_e32 v88, v3
	v_mov_b32_e32 v89, v3
	v_mov_b32_e32 v90, v3
	v_mov_b32_e32 v91, v3
	v_mov_b32_e32 v92, v3
	v_mov_b32_e32 v93, v3
	v_mov_b32_e32 v94, v3
	v_mov_b32_e32 v95, v3
	v_mov_b32_e32 v96, v3
	v_mov_b32_e32 v97, v3
	v_mov_b32_e32 v114, v3
	v_mov_b32_e32 v115, v3
	v_mov_b32_e32 v116, v3
	v_mov_b32_e32 v117, v3
	v_mov_b32_e32 v118, v3
	v_mov_b32_e32 v119, v3
	v_mov_b32_e32 v120, v3
	v_mov_b32_e32 v121, v3
	v_mov_b32_e32 v122, v3
	v_mov_b32_e32 v123, v3
	v_mov_b32_e32 v124, v3
	v_mov_b32_e32 v125, v3
	v_mov_b32_e32 v126, v3
	v_mov_b32_e32 v127, v3
	v_mov_b32_e32 v128, v3
	v_mov_b32_e32 v129, v3
	v_subrev_u32_e32 v136, s40, v136
	v_subrev_u32_e32 v138, s40, v138
	v_subrev_u32_e32 v140, s40, v140
	v_readfirstlane_b32 s62, v181
	s_add_u32 s44, s40, 0x1fa400
	s_addc_u32 s45, s41, 0
	s_add_u32 s46, s40, 0x219e40
	s_addc_u32 s47, s41, 0
	s_add_u32 s48, s40, 0x239880
	s_addc_u32 s49, s41, 0
	s_add_u32 s50, s40, 0x2592c0
	s_addc_u32 s51, s41, 0
	s_add_u32 s52, s40, 0x278d00
	s_addc_u32 s53, s41, 0
	s_add_u32 s54, s40, 0x298740
	s_addc_u32 s55, s41, 0
	s_add_u32 s56, s40, 0x2b8180
	s_addc_u32 s57, s41, 0
	s_add_u32 s58, s40, 0x2d7bc0
	s_addc_u32 s59, s41, 0
	s_barrier
	s_branch .LBB3_34
.LBB3_33:
	s_or_b64 exec, exec, s[26:27]
	v_lshl_add_u32 v142, v168, 4, s34
	v_lshl_add_u32 v200, v167, 4, s34
	ds_read_b128 v[188:191], v142
	ds_read_b128 v[192:195], v200
	ds_read_b128 v[196:199], v142 offset:2048
	ds_read_b128 v[200:203], v200 offset:2048
	ds_read_b128 v[204:207], v165 offset:57344
	ds_read_b128 v[208:211], v166 offset:57344
	v_lshl_add_u32 v142, v164, 4, s34
	v_lshl_add_u32 v232, v163, 4, s34
	s_add_u32 s60, s14, 0x18000
	s_addc_u32 s61, s15, 0
	s_add_u32 m0, s62, 0x6000
	s_nop 0
	global_load_lds_dwordx4 v130, s[60:61]
	s_add_u32 m0, s62, 0x8000
	s_nop 0
	global_load_lds_dwordx4 v132, s[60:61]
	s_add_u32 m0, s62, 0xa000
	s_nop 0
	global_load_lds_dwordx4 v134, s[60:61]
	s_add_u32 s44, s44, 0x1fa400
	s_addc_u32 s45, s45, 0
	s_add_u32 s46, s46, 0x1fa400
	s_addc_u32 s47, s47, 0
	s_add_u32 s48, s48, 0x1fa400
	s_addc_u32 s49, s49, 0
	s_add_u32 s50, s50, 0x1fa400
	s_addc_u32 s51, s51, 0
	s_add_u32 s52, s52, 0x1fa400
	s_addc_u32 s53, s53, 0
	s_add_u32 s54, s54, 0x1fa400
	s_addc_u32 s55, s55, 0
	s_add_u32 s56, s56, 0x1fa400
	s_addc_u32 s57, s57, 0
	s_add_u32 s58, s58, 0x1fa400
	s_addc_u32 s59, s59, 0
	s_cmp_lt_u32 s31, 30
	s_cselect_b64 s[26:27], -1, 0
	s_and_b64 s[36:37], s[26:27], s[10:11]
	v_mov_b32_e32 v143, 0
	v_mov_b32_e32 v187, 0
	v_mov_b32_e32 v186, 0
	v_mov_b32_e32 v185, 0
	v_mov_b32_e32 v147, 0
	v_mov_b32_e32 v145, 0
	v_mov_b32_e32 v144, 0
	v_mov_b32_e32 v146, 0
	s_and_saveexec_b64 s[26:27], s[36:37]
	global_load_dword v143, v140, s[44:45]
	global_load_dword v187, v140, s[46:47]
	global_load_dword v186, v140, s[48:49]
	global_load_dword v185, v140, s[50:51]
	global_load_dword v147, v140, s[52:53]
	global_load_dword v145, v140, s[54:55]
	global_load_dword v144, v140, s[56:57]
	global_load_dword v146, v140, s[58:59]
	s_mov_b64 exec, s[26:27]
	s_waitcnt lgkmcnt(0)
	v_mfma_f32_32x32x16_f16 v[98:113], v[204:207], v[188:191], v[98:113]
	ds_read_b128 v[212:215], v165 offset:59392
	ds_read_b128 v[216:219], v166 offset:59392
	s_add_u32 s12, s12, 0x1fa400
	s_addc_u32 s13, s13, 0
	s_add_u32 s14, s14, 0x12000
	s_addc_u32 s15, s15, 0
	s_cmp_eq_u32 s12, 0x3d4dc00
	v_mfma_f32_32x32x16_f16 v[114:129], v[204:207], v[192:195], v[114:129]
	ds_read_b128 v[220:223], v142
	ds_read_b128 v[224:227], v232
	s_mov_b32 s31, s33
	v_mfma_f32_32x32x16_f16 v[114:129], v[208:211], v[188:191], v[114:129]
	ds_read_b128 v[228:231], v142 offset:2048
	ds_read_b128 v[232:235], v232 offset:2048
	v_mfma_f32_32x32x16_f16 v[66:81], v[204:207], v[196:199], v[66:81]
	ds_read_b128 v[236:239], v161
	ds_read_b128 v[240:243], v162
	v_mfma_f32_32x32x16_f16 v[82:97], v[204:207], v[200:203], v[82:97]
	ds_read_b128 v[204:207], v159
	ds_read_b128 v[244:247], v160
	s_waitcnt lgkmcnt(0)
	s_barrier
	v_mfma_f32_32x32x16_f16 v[82:97], v[208:211], v[196:199], v[82:97]
	s_waitcnt lgkmcnt(0)
	v_mfma_f32_32x32x16_f16 v[34:49], v[212:215], v[188:191], v[34:49]
	v_mfma_f32_32x32x16_f16 v[50:65], v[212:215], v[192:195], v[50:65]
	v_mfma_f32_32x32x16_f16 v[50:65], v[216:219], v[188:191], v[50:65]
	v_mfma_f32_32x32x16_f16 v[2:17], v[212:215], v[196:199], v[2:17]
	v_mfma_f32_32x32x16_f16 v[18:33], v[212:215], v[200:203], v[18:33]
	v_mfma_f32_32x32x16_f16 v[18:33], v[216:219], v[196:199], v[18:33]
	v_mfma_f32_32x32x16_f16 v[98:113], v[236:239], v[220:223], v[98:113]
	v_mfma_f32_32x32x16_f16 v[114:129], v[236:239], v[224:227], v[114:129]
	v_mfma_f32_32x32x16_f16 v[114:129], v[240:243], v[220:223], v[114:129]
	v_mfma_f32_32x32x16_f16 v[66:81], v[236:239], v[228:231], v[66:81]
	v_mfma_f32_32x32x16_f16 v[82:97], v[236:239], v[232:235], v[82:97]
	v_mfma_f32_32x32x16_f16 v[82:97], v[240:243], v[228:231], v[82:97]
	v_mfma_f32_32x32x16_f16 v[34:49], v[204:207], v[220:223], v[34:49]
	v_mfma_f32_32x32x16_f16 v[50:65], v[204:207], v[224:227], v[50:65]
	v_mfma_f32_32x32x16_f16 v[50:65], v[244:247], v[220:223], v[50:65]
	v_mfma_f32_32x32x16_f16 v[2:17], v[204:207], v[228:231], v[2:17]
	v_mfma_f32_32x32x16_f16 v[18:33], v[204:207], v[232:235], v[18:33]
	v_mfma_f32_32x32x16_f16 v[18:33], v[244:247], v[228:231], v[18:33]
	s_cbranch_scc1 .LBB3_46
.LBB3_34:
	s_and_b32 s34, s31, 1
	s_mul_i32 s34, s34, 0x9b80
	v_lshl_add_u32 v142, v184, 4, s34
	v_lshl_add_u32 v200, v183, 4, s34
	ds_read_b128 v[188:191], v142
	ds_read_b128 v[192:195], v200
	ds_read_b128 v[196:199], v142 offset:2048
	ds_read_b128 v[200:203], v200 offset:2048
	s_waitcnt vmcnt(0)
	ds_read_b128 v[204:207], v165
	ds_read_b128 v[208:211], v166
	s_add_i32 s33, s31, 1
	s_and_b32 s35, s33, 1
	s_waitcnt lgkmcnt(0)
	v_mfma_f32_32x32x16_f16 v[98:113], v[204:207], v[188:191], v[98:113]
	ds_read_b128 v[212:215], v165 offset:2048
	ds_read_b128 v[216:219], v166 offset:2048
	s_waitcnt vmcnt(0)
	s_mul_i32 s35, s35, 0x9b80
	v_mfma_f32_32x32x16_f16 v[114:129], v[204:207], v[192:195], v[114:129]
	v_cvt_f16_f32_e32 v250, v143
	v_cvt_f16_f32_e32 v251, v187
	v_cvt_f32_f16_e32 v254, v250
	v_cvt_f32_f16_e32 v255, v251
	v_cmp_lt_f32_e64 s[36:37], |v254|, s30
	v_cmp_lt_f32_e64 s[38:39], |v255|, s30
	s_nop 0
	v_mfma_f32_32x32x16_f16 v[114:129], v[208:211], v[188:191], v[114:129]
	v_cndmask_b32_e64 v254, v254, 0, s[36:37]
	v_cndmask_b32_e64 v250, v250, 0, s[36:37]
	v_cndmask_b32_e64 v255, v255, 0, s[38:39]
	v_cndmask_b32_e64 v251, v251, 0, s[38:39]
	v_sub_f32_e32 v143, v143, v254
	v_sub_f32_e32 v187, v187, v255
	v_mul_f32_e32 v143, 0x45000000, v143
	v_mfma_f32_32x32x16_f16 v[66:81], v[204:207], v[196:199], v[66:81]
	v_mul_f32_e32 v187, 0x45000000, v187
	v_pack_b32_f16 v248, v250, v251
	v_cvt_pk_f16_f32 v252, v143, v187
	v_cvt_f16_f32_e32 v250, v186
	v_cvt_f16_f32_e32 v251, v185
	v_cvt_f32_f16_e32 v254, v250
	v_cvt_f32_f16_e32 v255, v251
	v_mfma_f32_32x32x16_f16 v[82:97], v[204:207], v[200:203], v[82:97]
	v_cmp_lt_f32_e64 s[36:37], |v254|, s30
	v_cmp_lt_f32_e64 s[38:39], |v255|, s30
	s_nop 0
	v_cndmask_b32_e64 v254, v254, 0, s[36:37]
	v_cndmask_b32_e64 v250, v250, 0, s[36:37]
	v_cndmask_b32_e64 v255, v255, 0, s[38:39]
	v_cndmask_b32_e64 v251, v251, 0, s[38:39]
	v_mfma_f32_32x32x16_f16 v[82:97], v[208:211], v[196:199], v[82:97]
	v_sub_f32_e32 v186, v186, v254
	v_sub_f32_e32 v185, v185, v255
	v_mul_f32_e32 v186, 0x45000000, v186
	v_mul_f32_e32 v185, 0x45000000, v185
	v_pack_b32_f16 v249, v250, v251
	v_cvt_pk_f16_f32 v253, v186, v185
	v_cvt_f16_f32_e32 v143, v147
	s_waitcnt lgkmcnt(1)
	v_mfma_f32_32x32x16_f16 v[34:49], v[212:215], v[188:191], v[34:49]
	v_cvt_f16_f32_e32 v187, v145
	v_cvt_f32_f16_e32 v186, v143
	v_cvt_f32_f16_e32 v185, v187
	v_cmp_lt_f32_e64 s[36:37], |v186|, s30
	v_cmp_lt_f32_e64 s[38:39], |v185|, s30
	s_nop 0
	v_cndmask_b32_e64 v186, v186, 0, s[36:37]
	v_mfma_f32_32x32x16_f16 v[50:65], v[212:215], v[192:195], v[50:65]
	v_cndmask_b32_e64 v143, v143, 0, s[36:37]
	v_cndmask_b32_e64 v185, v185, 0, s[38:39]
	v_cndmask_b32_e64 v187, v187, 0, s[38:39]
	v_sub_f32_e32 v147, v147, v186
	v_sub_f32_e32 v145, v145, v185
	v_mul_f32_e32 v147, 0x45000000, v147
	v_mul_f32_e32 v145, 0x45000000, v145
	s_waitcnt lgkmcnt(0)
	v_mfma_f32_32x32x16_f16 v[50:65], v[216:219], v[188:191], v[50:65]
	v_pack_b32_f16 v250, v143, v187
	v_cvt_pk_f16_f32 v254, v147, v145
	v_cvt_f16_f32_e32 v143, v144
	v_cvt_f16_f32_e32 v187, v146
	v_cvt_f32_f16_e32 v186, v143
	v_cvt_f32_f16_e32 v185, v187
	v_cmp_lt_f32_e64 s[36:37], |v186|, s30
	v_mfma_f32_32x32x16_f16 v[2:17], v[212:215], v[196:199], v[2:17]
	v_cmp_lt_f32_e64 s[38:39], |v185|, s30
	s_nop 0
	v_cndmask_b32_e64 v186, v186, 0, s[36:37]
	v_cndmask_b32_e64 v143, v143, 0, s[36:37]
	v_cndmask_b32_e64 v185, v185, 0, s[38:39]
	v_cndmask_b32_e64 v187, v187, 0, s[38:39]
	v_sub_f32_e32 v144, v144, v186
	v_mfma_f32_32x32x16_f16 v[18:33], v[212:215], v[200:203], v[18:33]
	v_sub_f32_e32 v146, v146, v185
	v_mul_f32_e32 v144, 0x45000000, v144
	v_mul_f32_e32 v146, 0x45000000, v146
	v_pack_b32_f16 v251, v143, v187
	v_cvt_pk_f16_f32 v255, v144, v146
	v_mfma_f32_32x32x16_f16 v[18:33], v[216:219], v[196:199], v[18:33]
	v_lshl_add_u32 v147, v152, 4, s35
	v_lshl_add_u32 v145, v1, 4, s35
	s_and_saveexec_b64 s[26:27], s[0:1]
	ds_write_b128 v147, v[248:251]
	ds_write_b128 v145, v[252:255]
	s_mov_b64 exec, s[26:27]
	v_lshl_add_u32 v193, v180, 4, s34
	v_lshl_add_u32 v206, v179, 4, s34
	ds_read_b128 v[194:197], v193
	ds_read_b128 v[198:201], v206
	ds_read_b128 v[202:205], v193 offset:2048
	ds_read_b128 v[206:209], v206 offset:2048
	ds_read_b128 v[210:213], v165 offset:8192
	ds_read_b128 v[214:217], v166 offset:8192
	v_lshl_add_u32 v193, v178, 4, s34
	s_add_u32 s60, s14, 0xc000
	s_addc_u32 s61, s15, 0
	s_add_u32 m0, s62, 0xc000
	s_nop 0
	global_load_lds_dwordx4 v130, s[60:61]
	s_add_u32 m0, s62, 0xe000
	s_nop 0
	global_load_lds_dwordx4 v132, s[60:61]
	s_add_u32 m0, s62, 0x10000
	s_nop 0
	global_load_lds_dwordx4 v134, s[60:61]
	v_mov_b32_e32 v143, 0
	v_mov_b32_e32 v187, 0
	v_mov_b32_e32 v186, 0
	v_mov_b32_e32 v185, 0
	v_mov_b32_e32 v147, 0
	v_mov_b32_e32 v145, 0
	v_mov_b32_e32 v144, 0
	v_mov_b32_e32 v146, 0
	s_and_saveexec_b64 s[26:27], s[6:7]
	global_load_dword v143, v136, s[44:45]
	global_load_dword v187, v136, s[46:47]
	global_load_dword v186, v136, s[48:49]
	global_load_dword v185, v136, s[50:51]
	global_load_dword v147, v136, s[52:53]
	global_load_dword v145, v136, s[54:55]
	global_load_dword v144, v136, s[56:57]
	global_load_dword v146, v136, s[58:59]
	s_mov_b64 exec, s[26:27]
	s_waitcnt lgkmcnt(0)
	v_mfma_f32_32x32x16_f16 v[98:113], v[210:213], v[194:197], v[98:113]
	ds_read_b128 v[218:221], v165 offset:10240
	ds_read_b128 v[222:225], v166 offset:10240
	v_mfma_f32_32x32x16_f16 v[114:129], v[210:213], v[198:201], v[114:129]
	v_mfma_f32_32x32x16_f16 v[114:129], v[214:217], v[194:197], v[114:129]
	v_mfma_f32_32x32x16_f16 v[66:81], v[210:213], v[202:205], v[66:81]
	v_mfma_f32_32x32x16_f16 v[82:97], v[210:213], v[206:209], v[82:97]
	ds_read_b128 v[210:213], v165 offset:16384
	v_mfma_f32_32x32x16_f16 v[82:97], v[214:217], v[202:205], v[82:97]
	ds_read_b128 v[214:217], v166 offset:16384
	s_waitcnt lgkmcnt(0)
	v_mfma_f32_32x32x16_f16 v[34:49], v[218:221], v[194:197], v[34:49]
	v_mfma_f32_32x32x16_f16 v[50:65], v[218:221], v[198:201], v[50:65]
	v_mfma_f32_32x32x16_f16 v[50:65], v[222:225], v[194:197], v[50:65]
	ds_read_b128 v[194:197], v193
	v_mfma_f32_32x32x16_f16 v[2:17], v[218:221], v[202:205], v[2:17]
	v_mfma_f32_32x32x16_f16 v[18:33], v[218:221], v[206:209], v[18:33]
	v_lshl_add_u32 v206, v177, 4, s34
	ds_read_b128 v[198:201], v206
	ds_read_b128 v[206:209], v206 offset:2048
	v_mfma_f32_32x32x16_f16 v[18:33], v[222:225], v[202:205], v[18:33]
	ds_read_b128 v[202:205], v193 offset:2048
	ds_read_b128 v[218:221], v165 offset:18432
	v_lshl_add_u32 v193, v176, 4, s34
	s_waitcnt lgkmcnt(0)
	v_mfma_f32_32x32x16_f16 v[98:113], v[210:213], v[194:197], v[98:113]
	ds_read_b128 v[222:225], v166 offset:18432
	s_waitcnt lgkmcnt(0)
	s_barrier
	v_mfma_f32_32x32x16_f16 v[114:129], v[210:213], v[198:201], v[114:129]
	v_mfma_f32_32x32x16_f16 v[114:129], v[214:217], v[194:197], v[114:129]
	v_mfma_f32_32x32x16_f16 v[66:81], v[210:213], v[202:205], v[66:81]
	v_mfma_f32_32x32x16_f16 v[82:97], v[210:213], v[206:209], v[82:97]
	ds_read_b128 v[210:213], v165 offset:24576
	v_mfma_f32_32x32x16_f16 v[82:97], v[214:217], v[202:205], v[82:97]
	ds_read_b128 v[214:217], v166 offset:24576
	v_mfma_f32_32x32x16_f16 v[34:49], v[218:221], v[194:197], v[34:49]
	v_mfma_f32_32x32x16_f16 v[50:65], v[218:221], v[198:201], v[50:65]
	s_waitcnt lgkmcnt(0)
	v_mfma_f32_32x32x16_f16 v[50:65], v[222:225], v[194:197], v[50:65]
	ds_read_b128 v[194:197], v193
	v_mfma_f32_32x32x16_f16 v[2:17], v[218:221], v[202:205], v[2:17]
	v_mfma_f32_32x32x16_f16 v[18:33], v[218:221], v[206:209], v[18:33]
	v_lshl_add_u32 v206, v175, 4, s34
	ds_read_b128 v[198:201], v206
	ds_read_b128 v[206:209], v206 offset:2048
	v_mfma_f32_32x32x16_f16 v[18:33], v[222:225], v[202:205], v[18:33]
	ds_read_b128 v[202:205], v193 offset:2048
	ds_read_b128 v[218:221], v165 offset:26624
	s_waitcnt lgkmcnt(0)
	v_mfma_f32_32x32x16_f16 v[98:113], v[210:213], v[194:197], v[98:113]
	ds_read_b128 v[222:225], v166 offset:26624
	s_waitcnt vmcnt(0)
	v_mfma_f32_32x32x16_f16 v[114:129], v[210:213], v[198:201], v[114:129]
	v_cvt_f16_f32_e32 v250, v143
	v_cvt_f16_f32_e32 v251, v187
	v_cvt_f32_f16_e32 v254, v250
	v_cvt_f32_f16_e32 v255, v251
	v_cmp_lt_f32_e64 s[36:37], |v254|, s30
	v_cmp_lt_f32_e64 s[38:39], |v255|, s30
	s_nop 0
	v_mfma_f32_32x32x16_f16 v[114:129], v[214:217], v[194:197], v[114:129]
	v_cndmask_b32_e64 v254, v254, 0, s[36:37]
	v_cndmask_b32_e64 v250, v250, 0, s[36:37]
	v_cndmask_b32_e64 v255, v255, 0, s[38:39]
	v_cndmask_b32_e64 v251, v251, 0, s[38:39]
	v_sub_f32_e32 v143, v143, v254
	v_sub_f32_e32 v187, v187, v255
	v_mul_f32_e32 v143, 0x45000000, v143
	v_mfma_f32_32x32x16_f16 v[66:81], v[210:213], v[202:205], v[66:81]
	v_mul_f32_e32 v187, 0x45000000, v187
	v_pack_b32_f16 v248, v250, v251
	v_cvt_pk_f16_f32 v252, v143, v187
	v_cvt_f16_f32_e32 v250, v186
	v_cvt_f16_f32_e32 v251, v185
	v_cvt_f32_f16_e32 v254, v250
	v_cvt_f32_f16_e32 v255, v251
	v_mfma_f32_32x32x16_f16 v[82:97], v[210:213], v[206:209], v[82:97]
	v_cmp_lt_f32_e64 s[36:37], |v254|, s30
	v_cmp_lt_f32_e64 s[38:39], |v255|, s30
	s_nop 0
	v_cndmask_b32_e64 v254, v254, 0, s[36:37]
	v_cndmask_b32_e64 v250, v250, 0, s[36:37]
	v_cndmask_b32_e64 v255, v255, 0, s[38:39]
	v_cndmask_b32_e64 v251, v251, 0, s[38:39]
	v_mfma_f32_32x32x16_f16 v[82:97], v[214:217], v[202:205], v[82:97]
	v_sub_f32_e32 v186, v186, v254
	v_sub_f32_e32 v185, v185, v255
	v_mul_f32_e32 v186, 0x45000000, v186
	v_mul_f32_e32 v185, 0x45000000, v185
	v_pack_b32_f16 v249, v250, v251
	v_cvt_pk_f16_f32 v253, v186, v185
	v_cvt_f16_f32_e32 v143, v147
	v_mfma_f32_32x32x16_f16 v[34:49], v[218:221], v[194:197], v[34:49]
	v_cvt_f16_f32_e32 v187, v145
	v_cvt_f32_f16_e32 v186, v143
	v_cvt_f32_f16_e32 v185, v187
	v_cmp_lt_f32_e64 s[36:37], |v186|, s30
	v_cmp_lt_f32_e64 s[38:39], |v185|, s30
	s_nop 0
	v_cndmask_b32_e64 v186, v186, 0, s[36:37]
	v_mfma_f32_32x32x16_f16 v[50:65], v[218:221], v[198:201], v[50:65]
	v_cndmask_b32_e64 v143, v143, 0, s[36:37]
	v_cndmask_b32_e64 v185, v185, 0, s[38:39]
	v_cndmask_b32_e64 v187, v187, 0, s[38:39]
	v_sub_f32_e32 v147, v147, v186
	v_sub_f32_e32 v145, v145, v185
	v_mul_f32_e32 v147, 0x45000000, v147
	v_mul_f32_e32 v145, 0x45000000, v145
	s_waitcnt lgkmcnt(0)
	v_mfma_f32_32x32x16_f16 v[50:65], v[222:225], v[194:197], v[50:65]
	v_pack_b32_f16 v250, v143, v187
	v_cvt_pk_f16_f32 v254, v147, v145
	v_cvt_f16_f32_e32 v143, v144
	v_cvt_f16_f32_e32 v187, v146
	v_cvt_f32_f16_e32 v186, v143
	v_cvt_f32_f16_e32 v185, v187
	v_cmp_lt_f32_e64 s[36:37], |v186|, s30
	v_mfma_f32_32x32x16_f16 v[2:17], v[218:221], v[202:205], v[2:17]
	v_cmp_lt_f32_e64 s[38:39], |v185|, s30
	s_nop 0
	v_cndmask_b32_e64 v186, v186, 0, s[36:37]
	v_cndmask_b32_e64 v143, v143, 0, s[36:37]
	v_cndmask_b32_e64 v185, v185, 0, s[38:39]
	v_cndmask_b32_e64 v187, v187, 0, s[38:39]
	v_sub_f32_e32 v144, v144, v186
	v_mfma_f32_32x32x16_f16 v[18:33], v[218:221], v[206:209], v[18:33]
	v_sub_f32_e32 v146, v146, v185
	v_mul_f32_e32 v144, 0x45000000, v144
	v_mul_f32_e32 v146, 0x45000000, v146
	v_pack_b32_f16 v251, v143, v187
	v_cvt_pk_f16_f32 v255, v144, v146
	v_mfma_f32_32x32x16_f16 v[18:33], v[222:225], v[202:205], v[18:33]
	v_lshl_add_u32 v147, v154, 4, s35
	v_lshl_add_u32 v145, v153, 4, s35
	s_and_saveexec_b64 s[26:27], s[2:3]
	ds_write_b128 v147, v[248:251]
	ds_write_b128 v145, v[252:255]
	s_mov_b64 exec, s[26:27]
	v_lshl_add_u32 v193, v174, 4, s34
	v_lshl_add_u32 v206, v173, 4, s34
	ds_read_b128 v[194:197], v193
	ds_read_b128 v[198:201], v206
	ds_read_b128 v[202:205], v193 offset:2048
	ds_read_b128 v[206:209], v206 offset:2048
	ds_read_b128 v[210:213], v165 offset:32768
	ds_read_b128 v[214:217], v166 offset:32768
	v_lshl_add_u32 v193, v172, 4, s34
	s_add_u32 s60, s14, 0x12000
	s_addc_u32 s61, s15, 0
	s_mov_b32 m0, s62
	s_nop 0
	global_load_lds_dwordx4 v130, s[60:61]
	s_add_u32 m0, s62, 0x2000
	s_nop 0
	global_load_lds_dwordx4 v132, s[60:61]
	s_add_u32 m0, s62, 0x4000
	s_nop 0
	global_load_lds_dwordx4 v134, s[60:61]
	v_mov_b32_e32 v143, 0
	v_mov_b32_e32 v187, 0
	v_mov_b32_e32 v186, 0
	v_mov_b32_e32 v185, 0
	v_mov_b32_e32 v147, 0
	v_mov_b32_e32 v145, 0
	v_mov_b32_e32 v144, 0
	v_mov_b32_e32 v146, 0
	s_and_saveexec_b64 s[26:27], s[8:9]
	global_load_dword v143, v138, s[44:45]
	global_load_dword v187, v138, s[46:47]
	global_load_dword v186, v138, s[48:49]
	global_load_dword v185, v138, s[50:51]
	global_load_dword v147, v138, s[52:53]
	global_load_dword v145, v138, s[54:55]
	global_load_dword v144, v138, s[56:57]
	global_load_dword v146, v138, s[58:59]
	s_mov_b64 exec, s[26:27]
	s_waitcnt lgkmcnt(0)
	v_mfma_f32_32x32x16_f16 v[98:113], v[210:213], v[194:197], v[98:113]
	ds_read_b128 v[218:221], v165 offset:34816
	ds_read_b128 v[222:225], v166 offset:34816
	v_mfma_f32_32x32x16_f16 v[114:129], v[210:213], v[198:201], v[114:129]
	v_mfma_f32_32x32x16_f16 v[114:129], v[214:217], v[194:197], v[114:129]
	v_mfma_f32_32x32x16_f16 v[66:81], v[210:213], v[202:205], v[66:81]
	v_mfma_f32_32x32x16_f16 v[82:97], v[210:213], v[206:209], v[82:97]
	ds_read_b128 v[210:213], v165 offset:40960
	v_mfma_f32_32x32x16_f16 v[82:97], v[214:217], v[202:205], v[82:97]
	ds_read_b128 v[214:217], v166 offset:40960
	s_waitcnt lgkmcnt(0)
	v_mfma_f32_32x32x16_f16 v[34:49], v[218:221], v[194:197], v[34:49]
	v_mfma_f32_32x32x16_f16 v[50:65], v[218:221], v[198:201], v[50:65]
	v_mfma_f32_32x32x16_f16 v[50:65], v[222:225], v[194:197], v[50:65]
	ds_read_b128 v[194:197], v193
	v_mfma_f32_32x32x16_f16 v[2:17], v[218:221], v[202:205], v[2:17]
	v_mfma_f32_32x32x16_f16 v[18:33], v[218:221], v[206:209], v[18:33]
	v_lshl_add_u32 v206, v171, 4, s34
	ds_read_b128 v[198:201], v206
	ds_read_b128 v[206:209], v206 offset:2048
	v_mfma_f32_32x32x16_f16 v[18:33], v[222:225], v[202:205], v[18:33]
	ds_read_b128 v[202:205], v193 offset:2048
	ds_read_b128 v[218:221], v165 offset:43008
	v_lshl_add_u32 v193, v170, 4, s34
	s_waitcnt lgkmcnt(0)
	v_mfma_f32_32x32x16_f16 v[98:113], v[210:213], v[194:197], v[98:113]
	ds_read_b128 v[222:225], v166 offset:43008
	s_waitcnt lgkmcnt(0)
	s_barrier
	v_mfma_f32_32x32x16_f16 v[114:129], v[210:213], v[198:201], v[114:129]
	v_mfma_f32_32x32x16_f16 v[114:129], v[214:217], v[194:197], v[114:129]
	v_mfma_f32_32x32x16_f16 v[66:81], v[210:213], v[202:205], v[66:81]
	v_mfma_f32_32x32x16_f16 v[82:97], v[210:213], v[206:209], v[82:97]
	s_waitcnt vmcnt(0)
	ds_read_b128 v[210:213], v165 offset:49152
	v_mfma_f32_32x32x16_f16 v[82:97], v[214:217], v[202:205], v[82:97]
	ds_read_b128 v[214:217], v166 offset:49152
	v_mfma_f32_32x32x16_f16 v[34:49], v[218:221], v[194:197], v[34:49]
	v_mfma_f32_32x32x16_f16 v[50:65], v[218:221], v[198:201], v[50:65]
	s_waitcnt lgkmcnt(2)
	v_mfma_f32_32x32x16_f16 v[50:65], v[222:225], v[194:197], v[50:65]
	ds_read_b128 v[194:197], v193
	v_mfma_f32_32x32x16_f16 v[2:17], v[218:221], v[202:205], v[2:17]
	v_mfma_f32_32x32x16_f16 v[18:33], v[218:221], v[206:209], v[18:33]
	v_lshl_add_u32 v206, v169, 4, s34
	ds_read_b128 v[198:201], v206
	ds_read_b128 v[206:209], v206 offset:2048
	v_mfma_f32_32x32x16_f16 v[18:33], v[222:225], v[202:205], v[18:33]
	ds_read_b128 v[202:205], v193 offset:2048
	ds_read_b128 v[218:221], v165 offset:51200
	s_waitcnt lgkmcnt(4)
	v_mfma_f32_32x32x16_f16 v[98:113], v[210:213], v[194:197], v[98:113]
	ds_read_b128 v[222:225], v166 offset:51200
	s_waitcnt vmcnt(0)
	s_waitcnt lgkmcnt(4)
	v_mfma_f32_32x32x16_f16 v[114:129], v[210:213], v[198:201], v[114:129]
	v_cvt_f16_f32_e32 v250, v143
	v_cvt_f16_f32_e32 v251, v187
	v_cvt_f32_f16_e32 v254, v250
	v_cvt_f32_f16_e32 v255, v251
	v_cmp_lt_f32_e64 s[36:37], |v254|, s30
	v_cmp_lt_f32_e64 s[38:39], |v255|, s30
	s_nop 0
	v_mfma_f32_32x32x16_f16 v[114:129], v[214:217], v[194:197], v[114:129]
	v_cndmask_b32_e64 v254, v254, 0, s[36:37]
	v_cndmask_b32_e64 v250, v250, 0, s[36:37]
	v_cndmask_b32_e64 v255, v255, 0, s[38:39]
	v_cndmask_b32_e64 v251, v251, 0, s[38:39]
	v_sub_f32_e32 v143, v143, v254
	v_sub_f32_e32 v187, v187, v255
	v_mul_f32_e32 v143, 0x45000000, v143
	s_waitcnt lgkmcnt(2)
	v_mfma_f32_32x32x16_f16 v[66:81], v[210:213], v[202:205], v[66:81]
	v_mul_f32_e32 v187, 0x45000000, v187
	v_pack_b32_f16 v248, v250, v251
	v_cvt_pk_f16_f32 v252, v143, v187
	v_cvt_f16_f32_e32 v250, v186
	v_cvt_f16_f32_e32 v251, v185
	v_cvt_f32_f16_e32 v254, v250
	v_cvt_f32_f16_e32 v255, v251
	v_mfma_f32_32x32x16_f16 v[82:97], v[210:213], v[206:209], v[82:97]
	v_cmp_lt_f32_e64 s[36:37], |v254|, s30
	v_cmp_lt_f32_e64 s[38:39], |v255|, s30
	s_nop 0
	v_cndmask_b32_e64 v254, v254, 0, s[36:37]
	v_cndmask_b32_e64 v250, v250, 0, s[36:37]
	v_cndmask_b32_e64 v255, v255, 0, s[38:39]
	v_cndmask_b32_e64 v251, v251, 0, s[38:39]
	v_mfma_f32_32x32x16_f16 v[82:97], v[214:217], v[202:205], v[82:97]
	v_sub_f32_e32 v186, v186, v254
	v_sub_f32_e32 v185, v185, v255
	v_mul_f32_e32 v186, 0x45000000, v186
	v_mul_f32_e32 v185, 0x45000000, v185
	v_pack_b32_f16 v249, v250, v251
	v_cvt_pk_f16_f32 v253, v186, v185
	v_cvt_f16_f32_e32 v143, v147
	s_waitcnt lgkmcnt(1)
	v_mfma_f32_32x32x16_f16 v[34:49], v[218:221], v[194:197], v[34:49]
	v_cvt_f16_f32_e32 v187, v145
	v_cvt_f32_f16_e32 v186, v143
	v_cvt_f32_f16_e32 v185, v187
	v_cmp_lt_f32_e64 s[36:37], |v186|, s30
	v_cmp_lt_f32_e64 s[38:39], |v185|, s30
	s_nop 0
	v_cndmask_b32_e64 v186, v186, 0, s[36:37]
	v_mfma_f32_32x32x16_f16 v[50:65], v[218:221], v[198:201], v[50:65]
	v_cndmask_b32_e64 v143, v143, 0, s[36:37]
	v_cndmask_b32_e64 v185, v185, 0, s[38:39]
	v_cndmask_b32_e64 v187, v187, 0, s[38:39]
	v_sub_f32_e32 v147, v147, v186
	v_sub_f32_e32 v145, v145, v185
	v_mul_f32_e32 v147, 0x45000000, v147
	v_mul_f32_e32 v145, 0x45000000, v145
	s_waitcnt lgkmcnt(0)
	v_mfma_f32_32x32x16_f16 v[50:65], v[222:225], v[194:197], v[50:65]
	v_pack_b32_f16 v250, v143, v187
	v_cvt_pk_f16_f32 v254, v147, v145
	v_cvt_f16_f32_e32 v143, v144
	v_cvt_f16_f32_e32 v187, v146
	v_cvt_f32_f16_e32 v186, v143
	v_cvt_f32_f16_e32 v185, v187
	v_cmp_lt_f32_e64 s[36:37], |v186|, s30
	v_mfma_f32_32x32x16_f16 v[2:17], v[218:221], v[202:205], v[2:17]
	v_cmp_lt_f32_e64 s[38:39], |v185|, s30
	s_nop 0
	v_cndmask_b32_e64 v186, v186, 0, s[36:37]
	v_cndmask_b32_e64 v143, v143, 0, s[36:37]
	v_cndmask_b32_e64 v185, v185, 0, s[38:39]
	v_cndmask_b32_e64 v187, v187, 0, s[38:39]
	v_sub_f32_e32 v144, v144, v186
	v_mfma_f32_32x32x16_f16 v[18:33], v[218:221], v[206:209], v[18:33]
	v_sub_f32_e32 v146, v146, v185
	v_mul_f32_e32 v144, 0x45000000, v144
	v_mul_f32_e32 v146, 0x45000000, v146
	v_pack_b32_f16 v251, v143, v187
	v_cvt_pk_f16_f32 v255, v144, v146
	v_mfma_f32_32x32x16_f16 v[18:33], v[222:225], v[202:205], v[18:33]
	v_lshl_add_u32 v147, v156, 4, s35
	v_lshl_add_u32 v145, v155, 4, s35
	s_and_saveexec_b64 s[26:27], s[4:5]
	ds_write_b128 v147, v[248:251]
	ds_write_b128 v145, v[252:255]
	s_mov_b64 exec, s[26:27]
	s_branch .LBB3_33

	.amdhsa_kernel _Z12conv1_kernelPKfPK15HIP_vector_typeIjLj4EES0_S0_S0_PDF16_
		.amdhsa_group_segment_fixed_size 154880
		.amdhsa_private_segment_fixed_size 0
		.amdhsa_kernarg_size 48
		.amdhsa_user_sgpr_count 2
		.amdhsa_user_sgpr_dispatch_ptr 0
		.amdhsa_user_sgpr_queue_ptr 0
		.amdhsa_user_sgpr_kernarg_segment_ptr 1
		.amdhsa_user_sgpr_dispatch_id 0
		.amdhsa_user_sgpr_kernarg_preload_length 0
		.amdhsa_user_sgpr_kernarg_preload_offset 0
		.amdhsa_user_sgpr_private_segment_size 0
		.amdhsa_uses_dynamic_stack 0
		.amdhsa_enable_private_segment 0
		.amdhsa_system_sgpr_workgroup_id_x 1
		.amdhsa_system_sgpr_workgroup_id_y 1
		.amdhsa_system_sgpr_workgroup_id_z 0
		.amdhsa_system_sgpr_workgroup_info 0
		.amdhsa_system_vgpr_workitem_id 0
		.amdhsa_next_free_vgpr 256
		.amdhsa_next_free_sgpr 96
		.amdhsa_accum_offset 256
		.amdhsa_reserve_vcc 1
		.amdhsa_float_round_mode_32 0
		.amdhsa_float_round_mode_16_64 0
		.amdhsa_float_denorm_mode_32 3
		.amdhsa_float_denorm_mode_16_64 3
		.amdhsa_dx10_clamp 1
		.amdhsa_ieee_mode 1
		.amdhsa_fp16_overflow 0
		.amdhsa_tg_split 0
		.amdhsa_exception_fp_ieee_invalid_op 0
		.amdhsa_exception_fp_denorm_src 0
		.amdhsa_exception_fp_ieee_div_zero 0
		.amdhsa_exception_fp_ieee_overflow 0
		.amdhsa_exception_fp_ieee_underflow 0
		.amdhsa_exception_fp_ieee_inexact 0
		.amdhsa_exception_int_div_zero 0
	.end_amdhsa_kernel

_Z15nms_hist_kernelPKfS0_PjS1_:
	s_load_dwordx8 s[4:11], s[0:1], 0x0
	v_lshlrev_b32_e32 v1, 4, v0
	v_mov_b32_e32 v2, 0
	v_mov_b32_e32 v3, 0
	v_mov_b32_e32 v4, 0
	v_mov_b32_e32 v5, 0
	ds_write_b128 v1, v[2:5] offset:0
	ds_write_b128 v1, v[2:5] offset:4096
	ds_write_b128 v1, v[2:5] offset:8192
	ds_write_b128 v1, v[2:5] offset:12288
	ds_write_b128 v1, v[2:5] offset:16384
	ds_write_b128 v1, v[2:5] offset:20480
	ds_write_b128 v1, v[2:5] offset:24576
	ds_write_b128 v1, v[2:5] offset:28672
	v_lshl_or_b32 v6, s2, 8, v0
	v_mov_b32_e32 v7, 1
	s_mov_b32 s80, 0x4f1a0
	s_mov_b32 s81, 0x4f19f
	s_mov_b32 s82, 530243
	s_mov_b32 s83, 32400
	s_mov_b32 s84, 46604
	s_movk_i32 s85, 180
	s_mov_b32 s86, 32220
	s_movk_i32 s87, 179
	s_movk_i32 s88, 178
	s_mul_i32 s18, s3, 0x13c680
	s_lshl_b32 s19, s3, 15
	s_waitcnt lgkmcnt(0)
	s_add_u32 s12, s4, s18
	s_addc_u32 s13, s5, 0
	s_add_u32 s14, s8, s18
	s_addc_u32 s15, s9, 0
	s_add_u32 s16, s10, s19
	s_addc_u32 s17, s11, 0
	v_mov_b32_e32 v112, v6
	v_cmp_gt_u32_e64 s[20:21], s80, v112
	v_min_u32_e32 v113, s81, v112
	v_mul_hi_u32 v114, v113, s82
	v_lshrrev_b32_e32 v114, 2, v114
	v_mul_u32_u24_e32 v115, s83, v114
	v_sub_u32_e32 v116, v113, v115
	v_mul_u32_u24_e32 v117, s84, v116
	v_lshrrev_b32_e32 v117, 23, v117
	v_mul_u32_u24_e32 v119, s85, v117
	v_sub_u32_e32 v120, v116, v119
	v_add_u32_e32 v125, -1, v117
	v_add_u32_e32 v123, -1, v120
	v_cmp_gt_u32_e64 s[18:19], s88, v125
	v_cmp_gt_u32_e64 vcc, s88, v123
	v_cmp_lt_u32_e64 s[22:23], 7, v114
	v_subrev_u32_e32 v121, s85, v119
	v_max_i32_e32 v121, 0, v121
	v_add_u32_e32 v122, s85, v119
	v_min_u32_e32 v122, s86, v122
	v_max_i32_e32 v123, 0, v123
	v_add_u32_e32 v124, 1, v120
	v_min_u32_e32 v124, s87, v124
	s_and_b64 s[18:19], s[18:19], vcc
	s_and_b64 s[24:25], s[18:19], s[20:21]
	s_and_b64 s[22:23], s[22:23], s[20:21]
	v_add_lshl_u32 v126, v115, v121, 2
	v_add_lshl_u32 v127, v115, v119, 2
	v_add_lshl_u32 v118, v115, v122, 2
	v_lshl_add_u32 v10, v123, 2, v126
	v_lshl_add_u32 v11, v120, 2, v126
	v_lshl_add_u32 v12, v124, 2, v126
	v_lshl_add_u32 v13, v123, 2, v127
	v_lshl_add_u32 v14, v124, 2, v127
	v_lshl_add_u32 v15, v123, 2, v118
	v_lshl_add_u32 v16, v120, 2, v118
	v_lshl_add_u32 v17, v124, 2, v118
	v_lshl_add_u32 v18, v120, 2, v127
	v_lshlrev_b32_e32 v19, 2, v114
	global_load_dword v10, v10, s[12:13]
	global_load_dword v11, v11, s[12:13]
	global_load_dword v12, v12, s[12:13]
	global_load_dword v13, v13, s[12:13]
	global_load_dword v14, v14, s[12:13]
	global_load_dword v15, v15, s[12:13]
	global_load_dword v16, v16, s[12:13]
	global_load_dword v17, v17, s[12:13]
	global_load_dword v18, v18, s[12:13]
	global_load_dword v19, v19, s[6:7]
	v_add_u32_e32 v112, 0x8000, v6
	v_cmp_gt_u32_e64 s[26:27], s80, v112
	v_min_u32_e32 v113, s81, v112
	v_mul_hi_u32 v114, v113, s82
	v_lshrrev_b32_e32 v114, 2, v114
	v_mul_u32_u24_e32 v115, s83, v114
	v_sub_u32_e32 v116, v113, v115
	v_mul_u32_u24_e32 v117, s84, v116
	v_lshrrev_b32_e32 v117, 23, v117
	v_mul_u32_u24_e32 v119, s85, v117
	v_sub_u32_e32 v120, v116, v119
	v_add_u32_e32 v125, -1, v117
	v_add_u32_e32 v123, -1, v120
	v_cmp_gt_u32_e64 s[18:19], s88, v125
	v_cmp_gt_u32_e64 vcc, s88, v123
	v_cmp_lt_u32_e64 s[28:29], 7, v114
	v_subrev_u32_e32 v121, s85, v119
	v_max_i32_e32 v121, 0, v121
	v_add_u32_e32 v122, s85, v119
	v_min_u32_e32 v122, s86, v122
	v_max_i32_e32 v123, 0, v123
	v_add_u32_e32 v124, 1, v120
	v_min_u32_e32 v124, s87, v124
	s_and_b64 s[18:19], s[18:19], vcc
	s_and_b64 s[30:31], s[18:19], s[26:27]
	s_and_b64 s[28:29], s[28:29], s[26:27]
	v_add_lshl_u32 v126, v115, v121, 2
	v_add_lshl_u32 v127, v115, v119, 2
	v_add_lshl_u32 v118, v115, v122, 2
	v_lshl_add_u32 v20, v123, 2, v126
	v_lshl_add_u32 v21, v120, 2, v126
	v_lshl_add_u32 v22, v124, 2, v126
	v_lshl_add_u32 v23, v123, 2, v127
	v_lshl_add_u32 v24, v124, 2, v127
	v_lshl_add_u32 v25, v123, 2, v118
	v_lshl_add_u32 v26, v120, 2, v118
	v_lshl_add_u32 v27, v124, 2, v118
	v_lshl_add_u32 v28, v120, 2, v127
	v_lshlrev_b32_e32 v29, 2, v114
	global_load_dword v20, v20, s[12:13]
	global_load_dword v21, v21, s[12:13]
	global_load_dword v22, v22, s[12:13]
	global_load_dword v23, v23, s[12:13]
	global_load_dword v24, v24, s[12:13]
	global_load_dword v25, v25, s[12:13]
	global_load_dword v26, v26, s[12:13]
	global_load_dword v27, v27, s[12:13]
	global_load_dword v28, v28, s[12:13]
	global_load_dword v29, v29, s[6:7]
	v_add_u32_e32 v112, 0x10000, v6
	v_cmp_gt_u32_e64 s[32:33], s80, v112
	v_min_u32_e32 v113, s81, v112
	v_mul_hi_u32 v114, v113, s82
	v_lshrrev_b32_e32 v114, 2, v114
	v_mul_u32_u24_e32 v115, s83, v114
	v_sub_u32_e32 v116, v113, v115
	v_mul_u32_u24_e32 v117, s84, v116
	v_lshrrev_b32_e32 v117, 23, v117
	v_mul_u32_u24_e32 v119, s85, v117
	v_sub_u32_e32 v120, v116, v119
	v_add_u32_e32 v125, -1, v117
	v_add_u32_e32 v123, -1, v120
	v_cmp_gt_u32_e64 s[18:19], s88, v125
	v_cmp_gt_u32_e64 vcc, s88, v123
	v_cmp_lt_u32_e64 s[34:35], 7, v114
	v_subrev_u32_e32 v121, s85, v119
	v_max_i32_e32 v121, 0, v121
	v_add_u32_e32 v122, s85, v119
	v_min_u32_e32 v122, s86, v122
	v_max_i32_e32 v123, 0, v123
	v_add_u32_e32 v124, 1, v120
	v_min_u32_e32 v124, s87, v124
	s_and_b64 s[18:19], s[18:19], vcc
	s_and_b64 s[36:37], s[18:19], s[32:33]
	s_and_b64 s[34:35], s[34:35], s[32:33]
	v_add_lshl_u32 v126, v115, v121, 2
	v_add_lshl_u32 v127, v115, v119, 2
	v_add_lshl_u32 v118, v115, v122, 2
	v_lshl_add_u32 v30, v123, 2, v126
	v_lshl_add_u32 v31, v120, 2, v126
	v_lshl_add_u32 v32, v124, 2, v126
	v_lshl_add_u32 v33, v123, 2, v127
	v_lshl_add_u32 v34, v124, 2, v127
	v_lshl_add_u32 v35, v123, 2, v118
	v_lshl_add_u32 v36, v120, 2, v118
	v_lshl_add_u32 v37, v124, 2, v118
	v_lshl_add_u32 v38, v120, 2, v127
	v_lshlrev_b32_e32 v39, 2, v114
	global_load_dword v30, v30, s[12:13]
	global_load_dword v31, v31, s[12:13]
	global_load_dword v32, v32, s[12:13]
	global_load_dword v33, v33, s[12:13]
	global_load_dword v34, v34, s[12:13]
	global_load_dword v35, v35, s[12:13]
	global_load_dword v36, v36, s[12:13]
	global_load_dword v37, v37, s[12:13]
	global_load_dword v38, v38, s[12:13]
	global_load_dword v39, v39, s[6:7]
	v_add_u32_e32 v112, 0x18000, v6
	v_cmp_gt_u32_e64 s[38:39], s80, v112
	v_min_u32_e32 v113, s81, v112
	v_mul_hi_u32 v114, v113, s82
	v_lshrrev_b32_e32 v114, 2, v114
	v_mul_u32_u24_e32 v115, s83, v114
	v_sub_u32_e32 v116, v113, v115
	v_mul_u32_u24_e32 v117, s84, v116
	v_lshrrev_b32_e32 v117, 23, v117
	v_mul_u32_u24_e32 v119, s85, v117
	v_sub_u32_e32 v120, v116, v119
	v_add_u32_e32 v125, -1, v117
	v_add_u32_e32 v123, -1, v120
	v_cmp_gt_u32_e64 s[18:19], s88, v125
	v_cmp_gt_u32_e64 vcc, s88, v123
	v_cmp_lt_u32_e64 s[40:41], 7, v114
	v_subrev_u32_e32 v121, s85, v119
	v_max_i32_e32 v121, 0, v121
	v_add_u32_e32 v122, s85, v119
	v_min_u32_e32 v122, s86, v122
	v_max_i32_e32 v123, 0, v123
	v_add_u32_e32 v124, 1, v120
	v_min_u32_e32 v124, s87, v124
	s_and_b64 s[18:19], s[18:19], vcc
	s_and_b64 s[42:43], s[18:19], s[38:39]
	s_and_b64 s[40:41], s[40:41], s[38:39]
	v_add_lshl_u32 v126, v115, v121, 2
	v_add_lshl_u32 v127, v115, v119, 2
	v_add_lshl_u32 v118, v115, v122, 2
	v_lshl_add_u32 v40, v123, 2, v126
	v_lshl_add_u32 v41, v120, 2, v126
	v_lshl_add_u32 v42, v124, 2, v126
	v_lshl_add_u32 v43, v123, 2, v127
	v_lshl_add_u32 v44, v124, 2, v127
	v_lshl_add_u32 v45, v123, 2, v118
	v_lshl_add_u32 v46, v120, 2, v118
	v_lshl_add_u32 v47, v124, 2, v118
	v_lshl_add_u32 v48, v120, 2, v127
	v_lshlrev_b32_e32 v49, 2, v114
	global_load_dword v40, v40, s[12:13]
	global_load_dword v41, v41, s[12:13]
	global_load_dword v42, v42, s[12:13]
	global_load_dword v43, v43, s[12:13]
	global_load_dword v44, v44, s[12:13]
	global_load_dword v45, v45, s[12:13]
	global_load_dword v46, v46, s[12:13]
	global_load_dword v47, v47, s[12:13]
	global_load_dword v48, v48, s[12:13]
	global_load_dword v49, v49, s[6:7]
	v_add_u32_e32 v112, 0x20000, v6
	v_cmp_gt_u32_e64 s[44:45], s80, v112
	v_min_u32_e32 v113, s81, v112
	v_mul_hi_u32 v114, v113, s82
	v_lshrrev_b32_e32 v114, 2, v114
	v_mul_u32_u24_e32 v115, s83, v114
	v_sub_u32_e32 v116, v113, v115
	v_mul_u32_u24_e32 v117, s84, v116
	v_lshrrev_b32_e32 v117, 23, v117
	v_mul_u32_u24_e32 v119, s85, v117
	v_sub_u32_e32 v120, v116, v119
	v_add_u32_e32 v125, -1, v117
	v_add_u32_e32 v123, -1, v120
	v_cmp_gt_u32_e64 s[18:19], s88, v125
	v_cmp_gt_u32_e64 vcc, s88, v123
	v_cmp_lt_u32_e64 s[46:47], 7, v114
	v_subrev_u32_e32 v121, s85, v119
	v_max_i32_e32 v121, 0, v121
	v_add_u32_e32 v122, s85, v119
	v_min_u32_e32 v122, s86, v122
	v_max_i32_e32 v123, 0, v123
	v_add_u32_e32 v124, 1, v120
	v_min_u32_e32 v124, s87, v124
	s_and_b64 s[18:19], s[18:19], vcc
	s_and_b64 s[48:49], s[18:19], s[44:45]
	s_and_b64 s[46:47], s[46:47], s[44:45]
	v_add_lshl_u32 v126, v115, v121, 2
	v_add_lshl_u32 v127, v115, v119, 2
	v_add_lshl_u32 v118, v115, v122, 2
	v_lshl_add_u32 v50, v123, 2, v126
	v_lshl_add_u32 v51, v120, 2, v126
	v_lshl_add_u32 v52, v124, 2, v126
	v_lshl_add_u32 v53, v123, 2, v127
	v_lshl_add_u32 v54, v124, 2, v127
	v_lshl_add_u32 v55, v123, 2, v118
	v_lshl_add_u32 v56, v120, 2, v118
	v_lshl_add_u32 v57, v124, 2, v118
	v_lshl_add_u32 v58, v120, 2, v127
	v_lshlrev_b32_e32 v59, 2, v114
	global_load_dword v50, v50, s[12:13]
	global_load_dword v51, v51, s[12:13]
	global_load_dword v52, v52, s[12:13]
	global_load_dword v53, v53, s[12:13]
	global_load_dword v54, v54, s[12:13]
	global_load_dword v55, v55, s[12:13]
	global_load_dword v56, v56, s[12:13]
	global_load_dword v57, v57, s[12:13]
	global_load_dword v58, v58, s[12:13]
	global_load_dword v59, v59, s[6:7]
	v_add_u32_e32 v112, 0x28000, v6
	v_cmp_gt_u32_e64 s[50:51], s80, v112
	v_min_u32_e32 v113, s81, v112
	v_mul_hi_u32 v114, v113, s82
	v_lshrrev_b32_e32 v114, 2, v114
	v_mul_u32_u24_e32 v115, s83, v114
	v_sub_u32_e32 v116, v113, v115
	v_mul_u32_u24_e32 v117, s84, v116
	v_lshrrev_b32_e32 v117, 23, v117
	v_mul_u32_u24_e32 v119, s85, v117
	v_sub_u32_e32 v120, v116, v119
	v_add_u32_e32 v125, -1, v117
	v_add_u32_e32 v123, -1, v120
	v_cmp_gt_u32_e64 s[18:19], s88, v125
	v_cmp_gt_u32_e64 vcc, s88, v123
	v_cmp_lt_u32_e64 s[52:53], 7, v114
	v_subrev_u32_e32 v121, s85, v119
	v_max_i32_e32 v121, 0, v121
	v_add_u32_e32 v122, s85, v119
	v_min_u32_e32 v122, s86, v122
	v_max_i32_e32 v123, 0, v123
	v_add_u32_e32 v124, 1, v120
	v_min_u32_e32 v124, s87, v124
	s_and_b64 s[18:19], s[18:19], vcc
	s_and_b64 s[54:55], s[18:19], s[50:51]
	s_and_b64 s[52:53], s[52:53], s[50:51]
	v_add_lshl_u32 v126, v115, v121, 2
	v_add_lshl_u32 v127, v115, v119, 2
	v_add_lshl_u32 v118, v115, v122, 2
	v_lshl_add_u32 v60, v123, 2, v126
	v_lshl_add_u32 v61, v120, 2, v126
	v_lshl_add_u32 v62, v124, 2, v126
	v_lshl_add_u32 v63, v123, 2, v127
	v_lshl_add_u32 v64, v124, 2, v127
	v_lshl_add_u32 v65, v123, 2, v118
	v_lshl_add_u32 v66, v120, 2, v118
	v_lshl_add_u32 v67, v124, 2, v118
	v_lshl_add_u32 v68, v120, 2, v127
	v_lshlrev_b32_e32 v69, 2, v114
	global_load_dword v60, v60, s[12:13]
	global_load_dword v61, v61, s[12:13]
	global_load_dword v62, v62, s[12:13]
	global_load_dword v63, v63, s[12:13]
	global_load_dword v64, v64, s[12:13]
	global_load_dword v65, v65, s[12:13]
	global_load_dword v66, v66, s[12:13]
	global_load_dword v67, v67, s[12:13]
	global_load_dword v68, v68, s[12:13]
	global_load_dword v69, v69, s[6:7]
	v_add_u32_e32 v112, 0x30000, v6
	v_cmp_gt_u32_e64 s[56:57], s80, v112
	v_min_u32_e32 v113, s81, v112
	v_mul_hi_u32 v114, v113, s82
	v_lshrrev_b32_e32 v114, 2, v114
	v_mul_u32_u24_e32 v115, s83, v114
	v_sub_u32_e32 v116, v113, v115
	v_mul_u32_u24_e32 v117, s84, v116
	v_lshrrev_b32_e32 v117, 23, v117
	v_mul_u32_u24_e32 v119, s85, v117
	v_sub_u32_e32 v120, v116, v119
	v_add_u32_e32 v125, -1, v117
	v_add_u32_e32 v123, -1, v120
	v_cmp_gt_u32_e64 s[18:19], s88, v125
	v_cmp_gt_u32_e64 vcc, s88, v123
	v_cmp_lt_u32_e64 s[58:59], 7, v114
	v_subrev_u32_e32 v121, s85, v119
	v_max_i32_e32 v121, 0, v121
	v_add_u32_e32 v122, s85, v119
	v_min_u32_e32 v122, s86, v122
	v_max_i32_e32 v123, 0, v123
	v_add_u32_e32 v124, 1, v120
	v_min_u32_e32 v124, s87, v124
	s_and_b64 s[18:19], s[18:19], vcc
	s_and_b64 s[60:61], s[18:19], s[56:57]
	s_and_b64 s[58:59], s[58:59], s[56:57]
	v_add_lshl_u32 v126, v115, v121, 2
	v_add_lshl_u32 v127, v115, v119, 2
	v_add_lshl_u32 v118, v115, v122, 2
	v_lshl_add_u32 v70, v123, 2, v126
	v_lshl_add_u32 v71, v120, 2, v126
	v_lshl_add_u32 v72, v124, 2, v126
	v_lshl_add_u32 v73, v123, 2, v127
	v_lshl_add_u32 v74, v124, 2, v127
	v_lshl_add_u32 v75, v123, 2, v118
	v_lshl_add_u32 v76, v120, 2, v118
	v_lshl_add_u32 v77, v124, 2, v118
	v_lshl_add_u32 v78, v120, 2, v127
	v_lshlrev_b32_e32 v79, 2, v114
	global_load_dword v70, v70, s[12:13]
	global_load_dword v71, v71, s[12:13]
	global_load_dword v72, v72, s[12:13]
	global_load_dword v73, v73, s[12:13]
	global_load_dword v74, v74, s[12:13]
	global_load_dword v75, v75, s[12:13]
	global_load_dword v76, v76, s[12:13]
	global_load_dword v77, v77, s[12:13]
	global_load_dword v78, v78, s[12:13]
	global_load_dword v79, v79, s[6:7]
	v_add_u32_e32 v112, 0x38000, v6
	v_cmp_gt_u32_e64 s[62:63], s80, v112
	v_min_u32_e32 v113, s81, v112
	v_mul_hi_u32 v114, v113, s82
	v_lshrrev_b32_e32 v114, 2, v114
	v_mul_u32_u24_e32 v115, s83, v114
	v_sub_u32_e32 v116, v113, v115
	v_mul_u32_u24_e32 v117, s84, v116
	v_lshrrev_b32_e32 v117, 23, v117
	v_mul_u32_u24_e32 v119, s85, v117
	v_sub_u32_e32 v120, v116, v119
	v_add_u32_e32 v125, -1, v117
	v_add_u32_e32 v123, -1, v120
	v_cmp_gt_u32_e64 s[18:19], s88, v125
	v_cmp_gt_u32_e64 vcc, s88, v123
	v_cmp_lt_u32_e64 s[64:65], 7, v114
	v_subrev_u32_e32 v121, s85, v119
	v_max_i32_e32 v121, 0, v121
	v_add_u32_e32 v122, s85, v119
	v_min_u32_e32 v122, s86, v122
	v_max_i32_e32 v123, 0, v123
	v_add_u32_e32 v124, 1, v120
	v_min_u32_e32 v124, s87, v124
	s_and_b64 s[18:19], s[18:19], vcc
	s_and_b64 s[66:67], s[18:19], s[62:63]
	s_and_b64 s[64:65], s[64:65], s[62:63]
	v_add_lshl_u32 v126, v115, v121, 2
	v_add_lshl_u32 v127, v115, v119, 2
	v_add_lshl_u32 v118, v115, v122, 2
	v_lshl_add_u32 v80, v123, 2, v126
	v_lshl_add_u32 v81, v120, 2, v126
	v_lshl_add_u32 v82, v124, 2, v126
	v_lshl_add_u32 v83, v123, 2, v127
	v_lshl_add_u32 v84, v124, 2, v127
	v_lshl_add_u32 v85, v123, 2, v118
	v_lshl_add_u32 v86, v120, 2, v118
	v_lshl_add_u32 v87, v124, 2, v118
	v_lshl_add_u32 v88, v120, 2, v127
	v_lshlrev_b32_e32 v89, 2, v114
	global_load_dword v80, v80, s[12:13]
	global_load_dword v81, v81, s[12:13]
	global_load_dword v82, v82, s[12:13]
	global_load_dword v83, v83, s[12:13]
	global_load_dword v84, v84, s[12:13]
	global_load_dword v85, v85, s[12:13]
	global_load_dword v86, v86, s[12:13]
	global_load_dword v87, v87, s[12:13]
	global_load_dword v88, v88, s[12:13]
	global_load_dword v89, v89, s[6:7]
	v_add_u32_e32 v112, 0x40000, v6
	v_cmp_gt_u32_e64 s[68:69], s80, v112
	v_min_u32_e32 v113, s81, v112
	v_mul_hi_u32 v114, v113, s82
	v_lshrrev_b32_e32 v114, 2, v114
	v_mul_u32_u24_e32 v115, s83, v114
	v_sub_u32_e32 v116, v113, v115
	v_mul_u32_u24_e32 v117, s84, v116
	v_lshrrev_b32_e32 v117, 23, v117
	v_mul_u32_u24_e32 v119, s85, v117
	v_sub_u32_e32 v120, v116, v119
	v_add_u32_e32 v125, -1, v117
	v_add_u32_e32 v123, -1, v120
	v_cmp_gt_u32_e64 s[18:19], s88, v125
	v_cmp_gt_u32_e64 vcc, s88, v123
	v_cmp_lt_u32_e64 s[70:71], 7, v114
	v_subrev_u32_e32 v121, s85, v119
	v_max_i32_e32 v121, 0, v121
	v_add_u32_e32 v122, s85, v119
	v_min_u32_e32 v122, s86, v122
	v_max_i32_e32 v123, 0, v123
	v_add_u32_e32 v124, 1, v120
	v_min_u32_e32 v124, s87, v124
	s_and_b64 s[18:19], s[18:19], vcc
	s_and_b64 s[72:73], s[18:19], s[68:69]
	s_and_b64 s[70:71], s[70:71], s[68:69]
	v_add_lshl_u32 v126, v115, v121, 2
	v_add_lshl_u32 v127, v115, v119, 2
	v_add_lshl_u32 v118, v115, v122, 2
	v_lshl_add_u32 v90, v123, 2, v126
	v_lshl_add_u32 v91, v120, 2, v126
	v_lshl_add_u32 v92, v124, 2, v126
	v_lshl_add_u32 v93, v123, 2, v127
	v_lshl_add_u32 v94, v124, 2, v127
	v_lshl_add_u32 v95, v123, 2, v118
	v_lshl_add_u32 v96, v120, 2, v118
	v_lshl_add_u32 v97, v124, 2, v118
	v_lshl_add_u32 v98, v120, 2, v127
	v_lshlrev_b32_e32 v99, 2, v114
	global_load_dword v90, v90, s[12:13]
	global_load_dword v91, v91, s[12:13]
	global_load_dword v92, v92, s[12:13]
	global_load_dword v93, v93, s[12:13]
	global_load_dword v94, v94, s[12:13]
	global_load_dword v95, v95, s[12:13]
	global_load_dword v96, v96, s[12:13]
	global_load_dword v97, v97, s[12:13]
	global_load_dword v98, v98, s[12:13]
	global_load_dword v99, v99, s[6:7]
	v_add_u32_e32 v112, 0x48000, v6
	v_cmp_gt_u32_e64 s[74:75], s80, v112
	v_min_u32_e32 v113, s81, v112
	v_mul_hi_u32 v114, v113, s82
	v_lshrrev_b32_e32 v114, 2, v114
	v_mul_u32_u24_e32 v115, s83, v114
	v_sub_u32_e32 v116, v113, v115
	v_mul_u32_u24_e32 v117, s84, v116
	v_lshrrev_b32_e32 v117, 23, v117
	v_mul_u32_u24_e32 v119, s85, v117
	v_sub_u32_e32 v120, v116, v119
	v_add_u32_e32 v125, -1, v117
	v_add_u32_e32 v123, -1, v120
	v_cmp_gt_u32_e64 s[18:19], s88, v125
	v_cmp_gt_u32_e64 vcc, s88, v123
	v_cmp_lt_u32_e64 s[76:77], 7, v114
	v_subrev_u32_e32 v121, s85, v119
	v_max_i32_e32 v121, 0, v121
	v_add_u32_e32 v122, s85, v119
	v_min_u32_e32 v122, s86, v122
	v_max_i32_e32 v123, 0, v123
	v_add_u32_e32 v124, 1, v120
	v_min_u32_e32 v124, s87, v124
	s_and_b64 s[18:19], s[18:19], vcc
	s_and_b64 s[78:79], s[18:19], s[74:75]
	s_and_b64 s[76:77], s[76:77], s[74:75]
	v_add_lshl_u32 v126, v115, v121, 2
	v_add_lshl_u32 v127, v115, v119, 2
	v_add_lshl_u32 v118, v115, v122, 2
	v_lshl_add_u32 v100, v123, 2, v126
	v_lshl_add_u32 v101, v120, 2, v126
	v_lshl_add_u32 v102, v124, 2, v126
	v_lshl_add_u32 v103, v123, 2, v127
	v_lshl_add_u32 v104, v124, 2, v127
	v_lshl_add_u32 v105, v123, 2, v118
	v_lshl_add_u32 v106, v120, 2, v118
	v_lshl_add_u32 v107, v124, 2, v118
	v_lshl_add_u32 v108, v120, 2, v127
	v_lshlrev_b32_e32 v109, 2, v114
	global_load_dword v100, v100, s[12:13]
	global_load_dword v101, v101, s[12:13]
	global_load_dword v102, v102, s[12:13]
	global_load_dword v103, v103, s[12:13]
	global_load_dword v104, v104, s[12:13]
	global_load_dword v105, v105, s[12:13]
	global_load_dword v106, v106, s[12:13]
	global_load_dword v107, v107, s[12:13]
	global_load_dword v108, v108, s[12:13]
	global_load_dword v109, v109, s[6:7]
	s_waitcnt lgkmcnt(0)
	s_barrier
	s_waitcnt vmcnt(63)
	v_max3_f32 v112, v10, v11, v12
	v_max3_f32 v112, v112, v13, v14
	v_max3_f32 v112, v112, v15, v16
	v_max_f32_e32 v112, v112, v17
	v_add_f32_e32 v113, v18, v19
	v_cmp_ge_f32_e64 s[18:19], v18, v112
	v_cmp_gt_i32_e32 vcc, 0, v113
	v_min_u32_e32 v114, -2, v113
	v_not_b32_e32 v114, v114
	v_or_b32_e32 v115, 0x80000000, v113
	s_and_b64 s[18:19], s[18:19], s[24:25]
	s_or_b64 s[18:19], s[18:19], s[22:23]
	v_cndmask_b32_e32 v115, v115, v114, vcc
	v_lshlrev_b32_e32 v117, 2, v6
	v_cndmask_b32_e64 v115, 0, v115, s[18:19]
	v_lshrrev_b32_e32 v116, 17, v115
	v_and_b32_e32 v116, 0x7ffc, v116
	s_mov_b64 exec, s[18:19]
	ds_add_u32 v116, v7
	s_mov_b64 exec, s[20:21]
	global_store_dword v117, v115, s[14:15]
	s_mov_b64 exec, -1
	s_waitcnt vmcnt(63)
	v_max3_f32 v112, v20, v21, v22
	v_max3_f32 v112, v112, v23, v24
	v_max3_f32 v112, v112, v25, v26
	v_max_f32_e32 v112, v112, v27
	v_add_f32_e32 v113, v28, v29
	v_cmp_ge_f32_e64 s[18:19], v28, v112
	v_cmp_gt_i32_e32 vcc, 0, v113
	v_min_u32_e32 v114, -2, v113
	v_not_b32_e32 v114, v114
	v_or_b32_e32 v115, 0x80000000, v113
	s_and_b64 s[18:19], s[18:19], s[30:31]
	s_or_b64 s[18:19], s[18:19], s[28:29]
	v_cndmask_b32_e32 v115, v115, v114, vcc
	v_add_u32_e32 v117, 0x8000, v6
	v_lshlrev_b32_e32 v117, 2, v117
	v_cndmask_b32_e64 v115, 0, v115, s[18:19]
	v_lshrrev_b32_e32 v116, 17, v115
	v_and_b32_e32 v116, 0x7ffc, v116
	s_mov_b64 exec, s[18:19]
	ds_add_u32 v116, v7
	s_mov_b64 exec, s[26:27]
	global_store_dword v117, v115, s[14:15]
	s_mov_b64 exec, -1
	s_waitcnt vmcnt(63)
	v_max3_f32 v112, v30, v31, v32
	v_max3_f32 v112, v112, v33, v34
	v_max3_f32 v112, v112, v35, v36
	v_max_f32_e32 v112, v112, v37
	v_add_f32_e32 v113, v38, v39
	v_cmp_ge_f32_e64 s[18:19], v38, v112
	v_cmp_gt_i32_e32 vcc, 0, v113
	v_min_u32_e32 v114, -2, v113
	v_not_b32_e32 v114, v114
	v_or_b32_e32 v115, 0x80000000, v113
	s_and_b64 s[18:19], s[18:19], s[36:37]
	s_or_b64 s[18:19], s[18:19], s[34:35]
	v_cndmask_b32_e32 v115, v115, v114, vcc
	v_add_u32_e32 v117, 0x10000, v6
	v_lshlrev_b32_e32 v117, 2, v117
	v_cndmask_b32_e64 v115, 0, v115, s[18:19]
	v_lshrrev_b32_e32 v116, 17, v115
	v_and_b32_e32 v116, 0x7ffc, v116
	s_mov_b64 exec, s[18:19]
	ds_add_u32 v116, v7
	s_mov_b64 exec, s[32:33]
	global_store_dword v117, v115, s[14:15]
	s_mov_b64 exec, -1
	s_waitcnt vmcnt(63)
	v_max3_f32 v112, v40, v41, v42
	v_max3_f32 v112, v112, v43, v44
	v_max3_f32 v112, v112, v45, v46
	v_max_f32_e32 v112, v112, v47
	v_add_f32_e32 v113, v48, v49
	v_cmp_ge_f32_e64 s[18:19], v48, v112
	v_cmp_gt_i32_e32 vcc, 0, v113
	v_min_u32_e32 v114, -2, v113
	v_not_b32_e32 v114, v114
	v_or_b32_e32 v115, 0x80000000, v113
	s_and_b64 s[18:19], s[18:19], s[42:43]
	s_or_b64 s[18:19], s[18:19], s[40:41]
	v_cndmask_b32_e32 v115, v115, v114, vcc
	v_add_u32_e32 v117, 0x18000, v6
	v_lshlrev_b32_e32 v117, 2, v117
	v_cndmask_b32_e64 v115, 0, v115, s[18:19]
	v_lshrrev_b32_e32 v116, 17, v115
	v_and_b32_e32 v116, 0x7ffc, v116
	s_mov_b64 exec, s[18:19]
	ds_add_u32 v116, v7
	s_mov_b64 exec, s[38:39]
	global_store_dword v117, v115, s[14:15]
	s_mov_b64 exec, -1
	s_waitcnt vmcnt(54)
	v_max3_f32 v112, v50, v51, v52
	v_max3_f32 v112, v112, v53, v54
	v_max3_f32 v112, v112, v55, v56
	v_max_f32_e32 v112, v112, v57
	v_add_f32_e32 v113, v58, v59
	v_cmp_ge_f32_e64 s[18:19], v58, v112
	v_cmp_gt_i32_e32 vcc, 0, v113
	v_min_u32_e32 v114, -2, v113
	v_not_b32_e32 v114, v114
	v_or_b32_e32 v115, 0x80000000, v113
	s_and_b64 s[18:19], s[18:19], s[48:49]
	s_or_b64 s[18:19], s[18:19], s[46:47]
	v_cndmask_b32_e32 v115, v115, v114, vcc
	v_add_u32_e32 v117, 0x20000, v6
	v_lshlrev_b32_e32 v117, 2, v117
	v_cndmask_b32_e64 v115, 0, v115, s[18:19]
	v_lshrrev_b32_e32 v116, 17, v115
	v_and_b32_e32 v116, 0x7ffc, v116
	s_mov_b64 exec, s[18:19]
	ds_add_u32 v116, v7
	s_mov_b64 exec, s[44:45]
	global_store_dword v117, v115, s[14:15]
	s_mov_b64 exec, -1
	s_waitcnt vmcnt(45)
	v_max3_f32 v112, v60, v61, v62
	v_max3_f32 v112, v112, v63, v64
	v_max3_f32 v112, v112, v65, v66
	v_max_f32_e32 v112, v112, v67
	v_add_f32_e32 v113, v68, v69
	v_cmp_ge_f32_e64 s[18:19], v68, v112
	v_cmp_gt_i32_e32 vcc, 0, v113
	v_min_u32_e32 v114, -2, v113
	v_not_b32_e32 v114, v114
	v_or_b32_e32 v115, 0x80000000, v113
	s_and_b64 s[18:19], s[18:19], s[54:55]
	s_or_b64 s[18:19], s[18:19], s[52:53]
	v_cndmask_b32_e32 v115, v115, v114, vcc
	v_add_u32_e32 v117, 0x28000, v6
	v_lshlrev_b32_e32 v117, 2, v117
	v_cndmask_b32_e64 v115, 0, v115, s[18:19]
	v_lshrrev_b32_e32 v116, 17, v115
	v_and_b32_e32 v116, 0x7ffc, v116
	s_mov_b64 exec, s[18:19]
	ds_add_u32 v116, v7
	s_mov_b64 exec, s[50:51]
	global_store_dword v117, v115, s[14:15]
	s_mov_b64 exec, -1
	s_waitcnt vmcnt(36)
	v_max3_f32 v112, v70, v71, v72
	v_max3_f32 v112, v112, v73, v74
	v_max3_f32 v112, v112, v75, v76
	v_max_f32_e32 v112, v112, v77
	v_add_f32_e32 v113, v78, v79
	v_cmp_ge_f32_e64 s[18:19], v78, v112
	v_cmp_gt_i32_e32 vcc, 0, v113
	v_min_u32_e32 v114, -2, v113
	v_not_b32_e32 v114, v114
	v_or_b32_e32 v115, 0x80000000, v113
	s_and_b64 s[18:19], s[18:19], s[60:61]
	s_or_b64 s[18:19], s[18:19], s[58:59]
	v_cndmask_b32_e32 v115, v115, v114, vcc
	v_add_u32_e32 v117, 0x30000, v6
	v_lshlrev_b32_e32 v117, 2, v117
	v_cndmask_b32_e64 v115, 0, v115, s[18:19]
	v_lshrrev_b32_e32 v116, 17, v115
	v_and_b32_e32 v116, 0x7ffc, v116
	s_mov_b64 exec, s[18:19]
	ds_add_u32 v116, v7
	s_mov_b64 exec, s[56:57]
	global_store_dword v117, v115, s[14:15]
	s_mov_b64 exec, -1
	s_waitcnt vmcnt(27)
	v_max3_f32 v112, v80, v81, v82
	v_max3_f32 v112, v112, v83, v84
	v_max3_f32 v112, v112, v85, v86
	v_max_f32_e32 v112, v112, v87
	v_add_f32_e32 v113, v88, v89
	v_cmp_ge_f32_e64 s[18:19], v88, v112
	v_cmp_gt_i32_e32 vcc, 0, v113
	v_min_u32_e32 v114, -2, v113
	v_not_b32_e32 v114, v114
	v_or_b32_e32 v115, 0x80000000, v113
	s_and_b64 s[18:19], s[18:19], s[66:67]
	s_or_b64 s[18:19], s[18:19], s[64:65]
	v_cndmask_b32_e32 v115, v115, v114, vcc
	v_add_u32_e32 v117, 0x38000, v6
	v_lshlrev_b32_e32 v117, 2, v117
	v_cndmask_b32_e64 v115, 0, v115, s[18:19]
	v_lshrrev_b32_e32 v116, 17, v115
	v_and_b32_e32 v116, 0x7ffc, v116
	s_mov_b64 exec, s[18:19]
	ds_add_u32 v116, v7
	s_mov_b64 exec, s[62:63]
	global_store_dword v117, v115, s[14:15]
	s_mov_b64 exec, -1
	s_waitcnt vmcnt(18)
	v_max3_f32 v112, v90, v91, v92
	v_max3_f32 v112, v112, v93, v94
	v_max3_f32 v112, v112, v95, v96
	v_max_f32_e32 v112, v112, v97
	v_add_f32_e32 v113, v98, v99
	v_cmp_ge_f32_e64 s[18:19], v98, v112
	v_cmp_gt_i32_e32 vcc, 0, v113
	v_min_u32_e32 v114, -2, v113
	v_not_b32_e32 v114, v114
	v_or_b32_e32 v115, 0x80000000, v113
	s_and_b64 s[18:19], s[18:19], s[72:73]
	s_or_b64 s[18:19], s[18:19], s[70:71]
	v_cndmask_b32_e32 v115, v115, v114, vcc
	v_add_u32_e32 v117, 0x40000, v6
	v_lshlrev_b32_e32 v117, 2, v117
	v_cndmask_b32_e64 v115, 0, v115, s[18:19]
	v_lshrrev_b32_e32 v116, 17, v115
	v_and_b32_e32 v116, 0x7ffc, v116
	s_mov_b64 exec, s[18:19]
	ds_add_u32 v116, v7
	s_mov_b64 exec, s[68:69]
	global_store_dword v117, v115, s[14:15]
	s_mov_b64 exec, -1
	s_waitcnt vmcnt(9)
	v_max3_f32 v112, v100, v101, v102
	v_max3_f32 v112, v112, v103, v104
	v_max3_f32 v112, v112, v105, v106
	v_max_f32_e32 v112, v112, v107
	v_add_f32_e32 v113, v108, v109
	v_cmp_ge_f32_e64 s[18:19], v108, v112
	v_cmp_gt_i32_e32 vcc, 0, v113
	v_min_u32_e32 v114, -2, v113
	v_not_b32_e32 v114, v114
	v_or_b32_e32 v115, 0x80000000, v113
	s_and_b64 s[18:19], s[18:19], s[78:79]
	s_or_b64 s[18:19], s[18:19], s[76:77]
	v_cndmask_b32_e32 v115, v115, v114, vcc
	v_add_u32_e32 v117, 0x48000, v6
	v_lshlrev_b32_e32 v117, 2, v117
	v_cndmask_b32_e64 v115, 0, v115, s[18:19]
	v_lshrrev_b32_e32 v116, 17, v115
	v_and_b32_e32 v116, 0x7ffc, v116
	s_mov_b64 exec, s[18:19]
	ds_add_u32 v116, v7
	s_mov_b64 exec, s[74:75]
	global_store_dword v117, v115, s[14:15]
	s_mov_b64 exec, -1
	s_waitcnt lgkmcnt(0)
	s_barrier
	v_lshlrev_b32_e32 v8, 2, v0
	ds_read_b32 v10, v8 offset:0
	ds_read_b32 v11, v8 offset:1024
	ds_read_b32 v12, v8 offset:2048
	ds_read_b32 v13, v8 offset:3072
	ds_read_b32 v14, v8 offset:4096
	ds_read_b32 v15, v8 offset:5120
	ds_read_b32 v16, v8 offset:6144
	ds_read_b32 v17, v8 offset:7168
	ds_read_b32 v18, v8 offset:8192
	ds_read_b32 v19, v8 offset:9216
	ds_read_b32 v20, v8 offset:10240
	ds_read_b32 v21, v8 offset:11264
	ds_read_b32 v22, v8 offset:12288
	ds_read_b32 v23, v8 offset:13312
	ds_read_b32 v24, v8 offset:14336
	ds_read_b32 v25, v8 offset:15360
	ds_read_b32 v26, v8 offset:16384
	ds_read_b32 v27, v8 offset:17408
	ds_read_b32 v28, v8 offset:18432
	ds_read_b32 v29, v8 offset:19456
	ds_read_b32 v30, v8 offset:20480
	ds_read_b32 v31, v8 offset:21504
	ds_read_b32 v32, v8 offset:22528
	ds_read_b32 v33, v8 offset:23552
	ds_read_b32 v34, v8 offset:24576
	ds_read_b32 v35, v8 offset:25600
	ds_read_b32 v36, v8 offset:26624
	ds_read_b32 v37, v8 offset:27648
	ds_read_b32 v38, v8 offset:28672
	ds_read_b32 v39, v8 offset:29696
	ds_read_b32 v40, v8 offset:30720
	ds_read_b32 v41, v8 offset:31744
	s_waitcnt lgkmcnt(0)
	v_cmp_ne_u32_e64 s[18:19], 0, v10
	s_nop 0
	s_mov_b64 exec, s[18:19]
	global_atomic_add v8, v10, s[16:17]
	s_mov_b64 exec, -1
	v_add_u32_e32 v8, 0x400, v8
	v_cmp_ne_u32_e64 s[18:19], 0, v11
	s_nop 0
	s_mov_b64 exec, s[18:19]
	global_atomic_add v8, v11, s[16:17]
	s_mov_b64 exec, -1
	v_add_u32_e32 v8, 0x400, v8
	v_cmp_ne_u32_e64 s[18:19], 0, v12
	s_nop 0
	s_mov_b64 exec, s[18:19]
	global_atomic_add v8, v12, s[16:17]
	s_mov_b64 exec, -1
	v_add_u32_e32 v8, 0x400, v8
	v_cmp_ne_u32_e64 s[18:19], 0, v13
	s_nop 0
	s_mov_b64 exec, s[18:19]
	global_atomic_add v8, v13, s[16:17]
	s_mov_b64 exec, -1
	v_add_u32_e32 v8, 0x400, v8
	v_cmp_ne_u32_e64 s[18:19], 0, v14
	s_nop 0
	s_mov_b64 exec, s[18:19]
	global_atomic_add v8, v14, s[16:17]
	s_mov_b64 exec, -1
	v_add_u32_e32 v8, 0x400, v8
	v_cmp_ne_u32_e64 s[18:19], 0, v15
	s_nop 0
	s_mov_b64 exec, s[18:19]
	global_atomic_add v8, v15, s[16:17]
	s_mov_b64 exec, -1
	v_add_u32_e32 v8, 0x400, v8
	v_cmp_ne_u32_e64 s[18:19], 0, v16
	s_nop 0
	s_mov_b64 exec, s[18:19]
	global_atomic_add v8, v16, s[16:17]
	s_mov_b64 exec, -1
	v_add_u32_e32 v8, 0x400, v8
	v_cmp_ne_u32_e64 s[18:19], 0, v17
	s_nop 0
	s_mov_b64 exec, s[18:19]
	global_atomic_add v8, v17, s[16:17]
	s_mov_b64 exec, -1
	v_add_u32_e32 v8, 0x400, v8
	v_cmp_ne_u32_e64 s[18:19], 0, v18
	s_nop 0
	s_mov_b64 exec, s[18:19]
	global_atomic_add v8, v18, s[16:17]
	s_mov_b64 exec, -1
	v_add_u32_e32 v8, 0x400, v8
	v_cmp_ne_u32_e64 s[18:19], 0, v19
	s_nop 0
	s_mov_b64 exec, s[18:19]
	global_atomic_add v8, v19, s[16:17]
	s_mov_b64 exec, -1
	v_add_u32_e32 v8, 0x400, v8
	v_cmp_ne_u32_e64 s[18:19], 0, v20
	s_nop 0
	s_mov_b64 exec, s[18:19]
	global_atomic_add v8, v20, s[16:17]
	s_mov_b64 exec, -1
	v_add_u32_e32 v8, 0x400, v8
	v_cmp_ne_u32_e64 s[18:19], 0, v21
	s_nop 0
	s_mov_b64 exec, s[18:19]
	global_atomic_add v8, v21, s[16:17]
	s_mov_b64 exec, -1
	v_add_u32_e32 v8, 0x400, v8
	v_cmp_ne_u32_e64 s[18:19], 0, v22
	s_nop 0
	s_mov_b64 exec, s[18:19]
	global_atomic_add v8, v22, s[16:17]
	s_mov_b64 exec, -1
	v_add_u32_e32 v8, 0x400, v8
	v_cmp_ne_u32_e64 s[18:19], 0, v23
	s_nop 0
	s_mov_b64 exec, s[18:19]
	global_atomic_add v8, v23, s[16:17]
	s_mov_b64 exec, -1
	v_add_u32_e32 v8, 0x400, v8
	v_cmp_ne_u32_e64 s[18:19], 0, v24
	s_nop 0
	s_mov_b64 exec, s[18:19]
	global_atomic_add v8, v24, s[16:17]
	s_mov_b64 exec, -1
	v_add_u32_e32 v8, 0x400, v8
	v_cmp_ne_u32_e64 s[18:19], 0, v25
	s_nop 0
	s_mov_b64 exec, s[18:19]
	global_atomic_add v8, v25, s[16:17]
	s_mov_b64 exec, -1
	v_add_u32_e32 v8, 0x400, v8
	v_cmp_ne_u32_e64 s[18:19], 0, v26
	s_nop 0
	s_mov_b64 exec, s[18:19]
	global_atomic_add v8, v26, s[16:17]
	s_mov_b64 exec, -1
	v_add_u32_e32 v8, 0x400, v8
	v_cmp_ne_u32_e64 s[18:19], 0, v27
	s_nop 0
	s_mov_b64 exec, s[18:19]
	global_atomic_add v8, v27, s[16:17]
	s_mov_b64 exec, -1
	v_add_u32_e32 v8, 0x400, v8
	v_cmp_ne_u32_e64 s[18:19], 0, v28
	s_nop 0
	s_mov_b64 exec, s[18:19]
	global_atomic_add v8, v28, s[16:17]
	s_mov_b64 exec, -1
	v_add_u32_e32 v8, 0x400, v8
	v_cmp_ne_u32_e64 s[18:19], 0, v29
	s_nop 0
	s_mov_b64 exec, s[18:19]
	global_atomic_add v8, v29, s[16:17]
	s_mov_b64 exec, -1
	v_add_u32_e32 v8, 0x400, v8
	v_cmp_ne_u32_e64 s[18:19], 0, v30
	s_nop 0
	s_mov_b64 exec, s[18:19]
	global_atomic_add v8, v30, s[16:17]
	s_mov_b64 exec, -1
	v_add_u32_e32 v8, 0x400, v8
	v_cmp_ne_u32_e64 s[18:19], 0, v31
	s_nop 0
	s_mov_b64 exec, s[18:19]
	global_atomic_add v8, v31, s[16:17]
	s_mov_b64 exec, -1
	v_add_u32_e32 v8, 0x400, v8
	v_cmp_ne_u32_e64 s[18:19], 0, v32
	s_nop 0
	s_mov_b64 exec, s[18:19]
	global_atomic_add v8, v32, s[16:17]
	s_mov_b64 exec, -1
	v_add_u32_e32 v8, 0x400, v8
	v_cmp_ne_u32_e64 s[18:19], 0, v33
	s_nop 0
	s_mov_b64 exec, s[18:19]
	global_atomic_add v8, v33, s[16:17]
	s_mov_b64 exec, -1
	v_add_u32_e32 v8, 0x400, v8
	v_cmp_ne_u32_e64 s[18:19], 0, v34
	s_nop 0
	s_mov_b64 exec, s[18:19]
	global_atomic_add v8, v34, s[16:17]
	s_mov_b64 exec, -1
	v_add_u32_e32 v8, 0x400, v8
	v_cmp_ne_u32_e64 s[18:19], 0, v35
	s_nop 0
	s_mov_b64 exec, s[18:19]
	global_atomic_add v8, v35, s[16:17]
	s_mov_b64 exec, -1
	v_add_u32_e32 v8, 0x400, v8
	v_cmp_ne_u32_e64 s[18:19], 0, v36
	s_nop 0
	s_mov_b64 exec, s[18:19]
	global_atomic_add v8, v36, s[16:17]
	s_mov_b64 exec, -1
	v_add_u32_e32 v8, 0x400, v8
	v_cmp_ne_u32_e64 s[18:19], 0, v37
	s_nop 0
	s_mov_b64 exec, s[18:19]
	global_atomic_add v8, v37, s[16:17]
	s_mov_b64 exec, -1
	v_add_u32_e32 v8, 0x400, v8
	v_cmp_ne_u32_e64 s[18:19], 0, v38
	s_nop 0
	s_mov_b64 exec, s[18:19]
	global_atomic_add v8, v38, s[16:17]
	s_mov_b64 exec, -1
	v_add_u32_e32 v8, 0x400, v8
	v_cmp_ne_u32_e64 s[18:19], 0, v39
	s_nop 0
	s_mov_b64 exec, s[18:19]
	global_atomic_add v8, v39, s[16:17]
	s_mov_b64 exec, -1
	v_add_u32_e32 v8, 0x400, v8
	v_cmp_ne_u32_e64 s[18:19], 0, v40
	s_nop 0
	s_mov_b64 exec, s[18:19]
	global_atomic_add v8, v40, s[16:17]
	s_mov_b64 exec, -1
	v_add_u32_e32 v8, 0x400, v8
	v_cmp_ne_u32_e64 s[18:19], 0, v41
	s_nop 0
	s_mov_b64 exec, s[18:19]
	global_atomic_add v8, v41, s[16:17]
	s_mov_b64 exec, -1
	s_endpgm

	.amdhsa_kernel _Z15nms_hist_kernelPKfS0_PjS1_
		.amdhsa_group_segment_fixed_size 32768
		.amdhsa_private_segment_fixed_size 0
		.amdhsa_kernarg_size 32
		.amdhsa_user_sgpr_count 2
		.amdhsa_user_sgpr_dispatch_ptr 0
		.amdhsa_user_sgpr_queue_ptr 0
		.amdhsa_user_sgpr_kernarg_segment_ptr 1
		.amdhsa_user_sgpr_dispatch_id 0
		.amdhsa_user_sgpr_kernarg_preload_length 0
		.amdhsa_user_sgpr_kernarg_preload_offset 0
		.amdhsa_user_sgpr_private_segment_size 0
		.amdhsa_uses_dynamic_stack 0
		.amdhsa_enable_private_segment 0
		.amdhsa_system_sgpr_workgroup_id_x 1
		.amdhsa_system_sgpr_workgroup_id_y 1
		.amdhsa_system_sgpr_workgroup_id_z 0
		.amdhsa_system_sgpr_workgroup_info 0
		.amdhsa_system_vgpr_workitem_id 0
		.amdhsa_next_free_vgpr 128
		.amdhsa_next_free_sgpr 96
		.amdhsa_accum_offset 128
		.amdhsa_reserve_vcc 1
		.amdhsa_float_round_mode_32 0
		.amdhsa_float_round_mode_16_64 0
		.amdhsa_float_denorm_mode_32 3
		.amdhsa_float_denorm_mode_16_64 3
		.amdhsa_dx10_clamp 1
		.amdhsa_ieee_mode 1
		.amdhsa_fp16_overflow 0
		.amdhsa_tg_split 0
		.amdhsa_exception_fp_ieee_invalid_op 0
		.amdhsa_exception_fp_denorm_src 0
		.amdhsa_exception_fp_ieee_div_zero 0
		.amdhsa_exception_fp_ieee_overflow 0
		.amdhsa_exception_fp_ieee_underflow 0
		.amdhsa_exception_fp_ieee_inexact 0
		.amdhsa_exception_int_div_zero 0
	.end_amdhsa_kernel

.LBB10_16:
	ds_read_b128 v[70:73], v66
	v_lshl_add_u32 v32, s11, 1, v61
	ds_read2_b64 v[56:59], v32 offset1:2
	ds_read2_b64 v[52:55], v32 offset0:4 offset1:6
	s_add_i32 s0, s10, s11
	s_cmpk_lt_i32 s0, 0x7e71
	s_waitcnt lgkmcnt(2)
	v_mfma_f32_32x32x16_f16 v[32:47], v[70:73], v[48:51], v[16:31]
	s_cbranch_scc1 .LBB10_18
	v_add_u32_e32 v69, s11, v67
	v_cmp_lt_i32_e32 vcc, s12, v69
	v_cmp_lt_i32_e64 s[0:1], s13, v69
	s_and_b64 vcc, s[0:1], vcc
	v_add_u32_e32 v70, 2, v69
	s_nop 5
	v_cndmask_b32_e32 v32, v32, v68, vcc
	v_cmp_gt_i32_e32 vcc, s14, v70
	v_add_u32_e32 v70, 3, v69
	v_cndmask_b32_e64 v33, v33, v68, s[0:1]
	v_cndmask_b32_e32 v34, v68, v34, vcc
	v_cmp_gt_i32_e32 vcc, s14, v70
	v_add_u32_e32 v70, 8, v69
	s_nop 0
	v_cndmask_b32_e32 v35, v68, v35, vcc
	v_cmp_gt_i32_e32 vcc, s14, v70
	v_add_u32_e32 v70, 9, v69
	s_nop 0
	v_cndmask_b32_e32 v36, v68, v36, vcc
	v_cmp_gt_i32_e32 vcc, s14, v70
	v_add_u32_e32 v70, 10, v69
	s_nop 0
	v_cndmask_b32_e32 v37, v68, v37, vcc
	v_cmp_gt_i32_e32 vcc, s14, v70
	v_add_u32_e32 v70, 11, v69
	s_nop 0
	v_cndmask_b32_e32 v38, v68, v38, vcc
	v_cmp_gt_i32_e32 vcc, s14, v70
	v_add_u32_e32 v70, 16, v69
	s_nop 0
	v_cndmask_b32_e32 v39, v68, v39, vcc
	v_cmp_gt_i32_e32 vcc, s14, v70
	v_add_u32_e32 v70, 17, v69
	s_nop 0
	v_cndmask_b32_e32 v40, v68, v40, vcc
	v_cmp_gt_i32_e32 vcc, s14, v70
	v_add_u32_e32 v70, 18, v69
	s_nop 0
	v_cndmask_b32_e32 v41, v68, v41, vcc
	v_cmp_gt_i32_e32 vcc, s14, v70
	v_add_u32_e32 v70, 19, v69
	s_nop 0
	v_cndmask_b32_e32 v42, v68, v42, vcc
	v_cmp_gt_i32_e32 vcc, s14, v70
	v_add_u32_e32 v70, 24, v69
	s_nop 0
	v_cndmask_b32_e32 v43, v68, v43, vcc
	v_cmp_gt_i32_e32 vcc, s14, v70
	v_add_u32_e32 v70, 25, v69
	s_nop 0
	v_cndmask_b32_e32 v44, v68, v44, vcc
	v_cmp_gt_i32_e32 vcc, s14, v70
	v_add_u32_e32 v70, 26, v69
	v_add_u32_e32 v69, 27, v69
	v_cndmask_b32_e32 v45, v68, v45, vcc
	v_cmp_gt_i32_e32 vcc, s14, v70
	s_nop 1
	v_cndmask_b32_e32 v46, v68, v46, vcc
	v_cmp_gt_i32_e32 vcc, s14, v69
	s_nop 1
	v_cndmask_b32_e32 v47, v68, v47, vcc
.LBB10_18:
	s_nop 10
	v_max3_f32 v69, v32, v33, v34
	v_max_f32_e32 v69, v69, v35
	v_max3_f32 v69, v69, v36, v37
	v_max3_f32 v69, v69, v38, v39
	v_max3_f32 v69, v69, v40, v41
	v_max3_f32 v69, v69, v42, v43
	v_max3_f32 v69, v69, v44, v45
	v_max3_f32 v69, v69, v46, v47
	v_cmp_lt_f32_e32 vcc, s15, v69
	s_cbranch_vccz .LBB10_15
	ds_bpermute_b32 v16, v63, v69
	v_mov_b32_e32 v18, v33
	v_mov_b32_e32 v19, v34
	v_mov_b32_e32 v20, v35
	v_mov_b32_e32 v21, v36
	s_waitcnt lgkmcnt(0)
	v_max3_f32 v30, v69, v16, 0
	v_exp_f32_e64 v16, -v30
	v_mov_b32_e32 v22, v37
	v_mov_b32_e32 v23, v38
	v_mov_b32_e32 v24, v39
	v_mov_b32_e32 v25, v40
	v_mov_b32_e32 v26, v41
	v_mov_b32_e32 v27, v42
	v_mov_b32_e32 v28, v43
	v_mov_b32_e32 v29, v44
	v_mov_b32_e32 v34, v45
	v_mov_b32_e32 v35, v46
	v_add_f32_e32 v64, v64, v30
	v_pk_mul_f32 v[0:1], v[16:17], v[0:1] op_sel_hi:[0,1]
	v_pk_mul_f32 v[2:3], v[16:17], v[2:3] op_sel_hi:[0,1]
	v_pk_mul_f32 v[4:5], v[16:17], v[4:5] op_sel_hi:[0,1]
	v_pk_mul_f32 v[6:7], v[16:17], v[6:7] op_sel_hi:[0,1]
	v_mul_f32_e32 v8, v16, v8
	v_xor_b32_e32 v16, 0x80000000, v64
	v_pk_add_f32 v[36:37], v[18:19], v[30:31] op_sel_hi:[1,0] neg_lo:[0,1] neg_hi:[0,1]
	v_pk_add_f32 v[38:39], v[20:21], v[30:31] op_sel_hi:[1,0] neg_lo:[0,1] neg_hi:[0,1]
	v_pk_add_f32 v[40:41], v[22:23], v[30:31] op_sel_hi:[1,0] neg_lo:[0,1] neg_hi:[0,1]
	v_pk_add_f32 v[42:43], v[24:25], v[30:31] op_sel_hi:[1,0] neg_lo:[0,1] neg_hi:[0,1]
	v_pk_add_f32 v[44:45], v[26:27], v[30:31] op_sel_hi:[1,0] neg_lo:[0,1] neg_hi:[0,1]
	v_pk_add_f32 v[70:71], v[28:29], v[30:31] op_sel_hi:[1,0] neg_lo:[0,1] neg_hi:[0,1]
	v_pk_add_f32 v[72:73], v[34:35], v[30:31] op_sel_hi:[1,0] neg_lo:[0,1] neg_hi:[0,1]
	v_sub_f32_e32 v32, v32, v30
	v_sub_f32_e32 v47, v47, v30
	v_mov_b32_e32 v17, v16
	v_mov_b32_e32 v18, v16
	v_mov_b32_e32 v19, v16
	v_mov_b32_e32 v20, v16
	v_mov_b32_e32 v21, v16
	v_mov_b32_e32 v22, v16
	v_mov_b32_e32 v23, v16
	v_mov_b32_e32 v24, v16
	v_mov_b32_e32 v25, v16
	v_mov_b32_e32 v26, v16
	v_mov_b32_e32 v27, v16
	v_mov_b32_e32 v28, v16
	v_mov_b32_e32 v29, v16
	v_mov_b32_e32 v30, v16
	v_mov_b32_e32 v31, v16
	v_mov_b32_e32 v33, v36
	v_mov_b32_e32 v34, v37
	v_mov_b32_e32 v35, v38
	v_mov_b32_e32 v36, v39
	v_mov_b32_e32 v37, v40
	v_mov_b32_e32 v38, v41
	v_mov_b32_e32 v39, v42
	v_mov_b32_e32 v40, v43
	v_mov_b32_e32 v41, v44
	v_mov_b32_e32 v42, v45
	v_mov_b32_e32 v43, v70
	v_mov_b32_e32 v44, v71
	v_mov_b32_e32 v45, v72
	v_mov_b32_e32 v46, v73
	s_branch .LBB10_15

	.text
	.p2alignl 8, 3212836864
	.fill 256, 4, 3212836864

amdhsa.kernels:
  - .agpr_count:     0
    .args:
      - .actual_access:  read_only
        .address_space:  global
        .offset:         0
        .size:           8
        .value_kind:     global_buffer
      - .actual_access:  write_only
        .address_space:  global
        .offset:         8
        .size:           8
        .value_kind:     global_buffer
    .group_segment_fixed_size: 0
    .kernarg_segment_align: 8
    .kernarg_segment_size: 16
    .language:       OpenCL C
    .language_version:
      - 2
      - 0
    .max_flat_workgroup_size: 256
    .name:           _Z13prep_x_kernelPKfP15HIP_vector_typeIjLj4EE
    .private_segment_fixed_size: 0
    .sgpr_count:     23
    .sgpr_spill_count: 0
    .symbol:         _Z13prep_x_kernelPKfP15HIP_vector_typeIjLj4EE.kd
    .uniform_work_group_size: 1
    .uses_dynamic_stack: false
    .vgpr_count:     36
    .vgpr_spill_count: 0
    .wavefront_size: 64
  - .agpr_count:     0
    .args:
      - .actual_access:  read_only
        .address_space:  global
        .offset:         0
        .size:           8
        .value_kind:     global_buffer
      - .actual_access:  write_only
        .address_space:  global
        .offset:         8
        .size:           8
        .value_kind:     global_buffer
      - .offset:         16
        .size:           4
        .value_kind:     by_value
      - .offset:         20
        .size:           4
        .value_kind:     by_value
      - .offset:         24
        .size:           4
        .value_kind:     by_value
      - .offset:         28
        .size:           4
        .value_kind:     by_value
    .group_segment_fixed_size: 0
    .kernarg_segment_align: 8
    .kernarg_segment_size: 32
    .language:       OpenCL C
    .language_version:
      - 2
      - 0
    .max_flat_workgroup_size: 256
    .name:           _Z13prep_w_kernelPKfP15HIP_vector_typeIjLj4EEiiii
    .private_segment_fixed_size: 0
    .sgpr_count:     15
    .sgpr_spill_count: 0
    .symbol:         _Z13prep_w_kernelPKfP15HIP_vector_typeIjLj4EEiiii.kd
    .uniform_work_group_size: 1
    .uses_dynamic_stack: false
    .vgpr_count:     34
    .vgpr_spill_count: 0
    .wavefront_size: 64
  - .agpr_count:     0
    .args:
      - .actual_access:  write_only
        .address_space:  global
        .offset:         0
        .size:           8
        .value_kind:     global_buffer
    .group_segment_fixed_size: 0
    .kernarg_segment_align: 8
    .kernarg_segment_size: 8
    .language:       OpenCL C
    .language_version:
      - 2
      - 0
    .max_flat_workgroup_size: 256
    .name:           _Z18zero_border_kernelP15HIP_vector_typeIjLj4EE
    .private_segment_fixed_size: 0
    .sgpr_count:     12
    .sgpr_spill_count: 0
    .symbol:         _Z18zero_border_kernelP15HIP_vector_typeIjLj4EE.kd
    .uniform_work_group_size: 1
    .uses_dynamic_stack: false
    .vgpr_count:     6
    .vgpr_spill_count: 0
    .wavefront_size: 64
  - .agpr_count:     0
    .args:
      - .actual_access:  read_only
        .address_space:  global
        .offset:         0
        .size:           8
        .value_kind:     global_buffer
      - .address_space:  global
        .offset:         8
        .size:           8
        .value_kind:     global_buffer
      - .actual_access:  read_only
        .address_space:  global
        .offset:         16
        .size:           8
        .value_kind:     global_buffer
      - .actual_access:  read_only
        .address_space:  global
        .offset:         24
        .size:           8
        .value_kind:     global_buffer
      - .actual_access:  read_only
        .address_space:  global
        .offset:         32
        .size:           8
        .value_kind:     global_buffer
      - .actual_access:  write_only
        .address_space:  global
        .offset:         40
        .size:           8
        .value_kind:     global_buffer
    .group_segment_fixed_size: 154880
    .kernarg_segment_align: 8
    .kernarg_segment_size: 48
    .language:       OpenCL C
    .language_version:
      - 2
      - 0
    .max_flat_workgroup_size: 512
    .name:           _Z12conv1_kernelPKfPK15HIP_vector_typeIjLj4EES0_S0_S0_PDF16_
    .private_segment_fixed_size: 0
    .sgpr_count:     46
    .sgpr_spill_count: 0
    .symbol:         _Z12conv1_kernelPKfPK15HIP_vector_typeIjLj4EES0_S0_S0_PDF16_.kd
    .uniform_work_group_size: 1
    .uses_dynamic_stack: false
    .vgpr_count:     256
    .vgpr_spill_count: 0
    .wavefront_size: 64
  - .agpr_count:     0
    .args:
      - .actual_access:  read_only
        .address_space:  global
        .offset:         0
        .size:           8
        .value_kind:     global_buffer
      - .actual_access:  read_only
        .address_space:  global
        .offset:         8
        .size:           8
        .value_kind:     global_buffer
      - .actual_access:  read_only
        .address_space:  global
        .offset:         16
        .size:           8
        .value_kind:     global_buffer
      - .actual_access:  write_only
        .address_space:  global
        .offset:         24
        .size:           8
        .value_kind:     global_buffer
      - .actual_access:  write_only
        .address_space:  global
        .offset:         32
        .size:           8
        .value_kind:     global_buffer
    .group_segment_fixed_size: 116480
    .kernarg_segment_align: 8
    .kernarg_segment_size: 40
    .language:       OpenCL C
    .language_version:
      - 2
      - 0
    .max_flat_workgroup_size: 512
    .name:           _Z12conv3_kernelPK15HIP_vector_typeIjLj4EES2_PKfPfS5_
    .private_segment_fixed_size: 0
    .sgpr_count:     22
    .sgpr_spill_count: 0
    .symbol:         _Z12conv3_kernelPK15HIP_vector_typeIjLj4EES2_PKfPfS5_.kd
    .uniform_work_group_size: 1
    .uses_dynamic_stack: false
    .vgpr_count:     122
    .vgpr_spill_count: 0
    .wavefront_size: 64
  - .agpr_count:     0
    .args:
      - .actual_access:  read_only
        .address_space:  global
        .offset:         0
        .size:           8
        .value_kind:     global_buffer
      - .actual_access:  read_only
        .address_space:  global
        .offset:         8
        .size:           8
        .value_kind:     global_buffer
      - .actual_access:  write_only
        .address_space:  global
        .offset:         16
        .size:           8
        .value_kind:     global_buffer
      - .address_space:  global
        .offset:         24
        .size:           8
        .value_kind:     global_buffer
    .group_segment_fixed_size: 32768
    .kernarg_segment_align: 8
    .kernarg_segment_size: 32
    .language:       OpenCL C
    .language_version:
      - 2
      - 0
    .max_flat_workgroup_size: 256
    .name:           _Z15nms_hist_kernelPKfS0_PjS1_
    .private_segment_fixed_size: 0
    .sgpr_count:     102
    .sgpr_spill_count: 0
    .symbol:         _Z15nms_hist_kernelPKfS0_PjS1_.kd
    .uniform_work_group_size: 1
    .uses_dynamic_stack: false
    .vgpr_count:     128
    .vgpr_spill_count: 0
    .wavefront_size: 64
  - .agpr_count:     0
    .args:
      - .actual_access:  read_only
        .address_space:  global
        .offset:         0
        .size:           8
        .value_kind:     global_buffer
      - .actual_access:  write_only
        .address_space:  global
        .offset:         8
        .size:           8
        .value_kind:     global_buffer
    .group_segment_fixed_size: 4096
    .kernarg_segment_align: 8
    .kernarg_segment_size: 16
    .language:       OpenCL C
    .language_version:
      - 2
      - 0
    .max_flat_workgroup_size: 1024
    .name:           _Z17select_bin_kernelPKjPi
    .private_segment_fixed_size: 0
    .sgpr_count:     23
    .sgpr_spill_count: 0
    .symbol:         _Z17select_bin_kernelPKjPi.kd
    .uniform_work_group_size: 1
    .uses_dynamic_stack: false
    .vgpr_count:     13
    .vgpr_spill_count: 0
    .wavefront_size: 64
  - .agpr_count:     0
    .args:
      - .actual_access:  read_only
        .address_space:  global
        .offset:         0
        .size:           8
        .value_kind:     global_buffer
      - .actual_access:  read_only
        .address_space:  global
        .offset:         8
        .size:           8
        .value_kind:     global_buffer
      - .address_space:  global
        .offset:         16
        .size:           8
        .value_kind:     global_buffer
      - .actual_access:  write_only
        .address_space:  global
        .offset:         24
        .size:           8
        .value_kind:     global_buffer
    .group_segment_fixed_size: 2052
    .kernarg_segment_align: 8
    .kernarg_segment_size: 32
    .language:       OpenCL C
    .language_version:
      - 2
      - 0
    .max_flat_workgroup_size: 512
    .name:           _Z14collect_kernelPKjS0_PiS1_
    .private_segment_fixed_size: 0
    .sgpr_count:     19
    .sgpr_spill_count: 0
    .symbol:         _Z14collect_kernelPKjS0_PiS1_.kd
    .uniform_work_group_size: 1
    .uses_dynamic_stack: false
    .vgpr_count:     34
    .vgpr_spill_count: 0
    .wavefront_size: 64
  - .agpr_count:     0
    .args:
      - .actual_access:  read_only
        .address_space:  global
        .offset:         0
        .size:           8
        .value_kind:     global_buffer
      - .actual_access:  read_only
        .address_space:  global
        .offset:         8
        .size:           8
        .value_kind:     global_buffer
      - .actual_access:  read_only
        .address_space:  global
        .offset:         16
        .size:           8
        .value_kind:     global_buffer
      - .actual_access:  read_only
        .address_space:  global
        .offset:         24
        .size:           8
        .value_kind:     global_buffer
      - .actual_access:  write_only
        .address_space:  global
        .offset:         32
        .size:           8
        .value_kind:     global_buffer
    .group_segment_fixed_size: 49664
    .kernarg_segment_align: 8
    .kernarg_segment_size: 40
    .language:       OpenCL C
    .language_version:
      - 2
      - 0
    .max_flat_workgroup_size: 1024
    .name:           _Z11rank_kernelPKfS0_PKiS2_Pi
    .private_segment_fixed_size: 0
    .sgpr_count:     23
    .sgpr_spill_count: 0
    .symbol:         _Z11rank_kernelPKfS0_PKiS2_Pi.kd
    .uniform_work_group_size: 1
    .uses_dynamic_stack: false
    .vgpr_count:     12
    .vgpr_spill_count: 0
    .wavefront_size: 64
  - .agpr_count:     0
    .args:
      - .actual_access:  read_only
        .address_space:  global
        .offset:         0
        .size:           8
        .value_kind:     global_buffer
      - .actual_access:  read_only
        .address_space:  global
        .offset:         8
        .size:           8
        .value_kind:     global_buffer
      - .actual_access:  write_only
        .address_space:  global
        .offset:         16
        .size:           8
        .value_kind:     global_buffer
      - .actual_access:  write_only
        .address_space:  global
        .offset:         24
        .size:           8
        .value_kind:     global_buffer
    .group_segment_fixed_size: 0
    .kernarg_segment_align: 8
    .kernarg_segment_size: 32
    .language:       OpenCL C
    .language_version:
      - 2
      - 0
    .max_flat_workgroup_size: 256
    .name:           _Z15prep_kvw_kernelPKfS0_PDF16_S1_
    .private_segment_fixed_size: 0
    .sgpr_count:     14
    .sgpr_spill_count: 0
    .symbol:         _Z15prep_kvw_kernelPKfS0_PDF16_S1_.kd
    .uniform_work_group_size: 1
    .uses_dynamic_stack: false
    .vgpr_count:     7
    .vgpr_spill_count: 0
    .wavefront_size: 64
  - .agpr_count:     0
    .args:
      - .actual_access:  read_only
        .address_space:  global
        .offset:         0
        .size:           8
        .value_kind:     global_buffer
      - .actual_access:  read_only
        .address_space:  global
        .offset:         8
        .size:           8
        .value_kind:     global_buffer
      - .actual_access:  read_only
        .address_space:  global
        .offset:         16
        .size:           8
        .value_kind:     global_buffer
      - .actual_access:  read_only
        .address_space:  global
        .offset:         24
        .size:           8
        .value_kind:     global_buffer
      - .actual_access:  write_only
        .address_space:  global
        .offset:         32
        .size:           8
        .value_kind:     global_buffer
    .group_segment_fixed_size: 67856
    .kernarg_segment_align: 8
    .kernarg_segment_size: 40
    .language:       OpenCL C
    .language_version:
      - 2
      - 0
    .max_flat_workgroup_size: 448
    .name:           _Z17cross_attn_kernelPKDF16_S0_S0_S0_Pf
    .private_segment_fixed_size: 0
    .sgpr_count:     26
    .sgpr_spill_count: 0
    .symbol:         _Z17cross_attn_kernelPKDF16_S0_S0_S0_Pf.kd
    .uniform_work_group_size: 1
    .uses_dynamic_stack: false
    .vgpr_count:     74
    .vgpr_spill_count: 0
    .wavefront_size: 64
  - .agpr_count:     0
    .args:
      - .offset:         0
        .size:           424
        .value_kind:     by_value
      - .offset:         424
        .size:           88
        .value_kind:     by_value
    .group_segment_fixed_size: 137216
    .kernarg_segment_align: 8
    .kernarg_segment_size: 512
    .language:       OpenCL C
    .language_version:
      - 2
      - 0
    .max_flat_workgroup_size: 512
    .name:           _Z12tailA_kernel5TailP3KvP
    .private_segment_fixed_size: 0
    .sgpr_count:     44
    .sgpr_spill_count: 0
    .symbol:         _Z12tailA_kernel5TailP3KvP.kd
    .uniform_work_group_size: 1
    .uses_dynamic_stack: false
    .vgpr_count:     184
    .vgpr_spill_count: 0
    .wavefront_size: 64
  - .agpr_count:     0
    .args:
      - .offset:         0
        .size:           424
        .value_kind:     by_value
      - .offset:         424
        .size:           88
        .value_kind:     by_value
    .group_segment_fixed_size: 146592
    .kernarg_segment_align: 8
    .kernarg_segment_size: 512
    .language:       OpenCL C
    .language_version:
      - 2
      - 0
    .max_flat_workgroup_size: 512
    .name:           _Z12tailB_kernel5TailP3KvP
    .private_segment_fixed_size: 0
    .sgpr_count:     44
    .sgpr_spill_count: 0
    .symbol:         _Z12tailB_kernel5TailP3KvP.kd
    .uniform_work_group_size: 1
    .uses_dynamic_stack: false
    .vgpr_count:     216
    .vgpr_spill_count: 0
    .wavefront_size: 64
  - .agpr_count:     0
    .args:
      - .offset:         0
        .size:           424
        .value_kind:     by_value
    .group_segment_fixed_size: 36896
    .kernarg_segment_align: 8
    .kernarg_segment_size: 424
    .language:       OpenCL C
    .language_version:
      - 2
      - 0
    .max_flat_workgroup_size: 512
    .name:           _Z12tailC_kernel5TailP
    .private_segment_fixed_size: 0
    .sgpr_count:     58
    .sgpr_spill_count: 0
    .symbol:         _Z12tailC_kernel5TailP.kd
    .uniform_work_group_size: 1
    .uses_dynamic_stack: false
    .vgpr_count:     113
    .vgpr_spill_count: 0
    .wavefront_size: 64
  - .agpr_count:     0
    .args:
      - .offset:         0
        .size:           344
        .value_kind:     by_value
    .group_segment_fixed_size: 0
    .kernarg_segment_align: 8
    .kernarg_segment_size: 344
    .language:       OpenCL C
    .language_version:
      - 2
      - 0
    .max_flat_workgroup_size: 256
    .name:           _Z15prep_all_kernel5PrepP
    .private_segment_fixed_size: 0
    .sgpr_count:     31
    .sgpr_spill_count: 0
    .symbol:         _Z15prep_all_kernel5PrepP.kd
    .uniform_work_group_size: 1
    .uses_dynamic_stack: false
    .vgpr_count:     39
    .vgpr_spill_count: 0
    .wavefront_size: 64
  - .agpr_count:     0
    .args:
      - .actual_access:  read_only
        .address_space:  global
        .offset:         0
        .size:           8
        .value_kind:     global_buffer
      - .actual_access:  read_only
        .address_space:  global
        .offset:         8
        .size:           8
        .value_kind:     global_buffer
      - .actual_access:  read_only
        .address_space:  global
        .offset:         16
        .size:           8
        .value_kind:     global_buffer
      - .actual_access:  read_only
        .address_space:  global
        .offset:         24
        .size:           8
        .value_kind:     global_buffer
      - .actual_access:  read_only
        .address_space:  global
        .offset:         32
        .size:           8
        .value_kind:     global_buffer
      - .actual_access:  write_only
        .address_space:  global
        .offset:         40
        .size:           8
        .value_kind:     global_buffer
      - .actual_access:  read_only
        .address_space:  global
        .offset:         48
        .size:           8
        .value_kind:     global_buffer
      - .actual_access:  read_only
        .address_space:  global
        .offset:         56
        .size:           8
        .value_kind:     global_buffer
    .group_segment_fixed_size: 130304
    .kernarg_segment_align: 8
    .kernarg_segment_size: 64
    .language:       OpenCL C
    .language_version:
      - 2
      - 0
    .max_flat_workgroup_size: 512
    .name:           _Z11conv_kernelILi8ELi128ELi0EEvPK15HIP_vector_typeIjLj4EES3_PKfS5_S5_PDF16_PfS7_
    .private_segment_fixed_size: 0
    .sgpr_count:     30
    .sgpr_spill_count: 0
    .symbol:         _Z11conv_kernelILi8ELi128ELi0EEvPK15HIP_vector_typeIjLj4EES3_PKfS5_S5_PDF16_PfS7_.kd
    .uniform_work_group_size: 1
    .uses_dynamic_stack: false
    .vgpr_count:     254
    .vgpr_spill_count: 0
    .wavefront_size: 64
